# speedup vs baseline: 1.0342x; 1.0162x over previous
_Z11pwconv_mfmaPKfPK15HIP_vector_typeIjLj4EES0_Pf:
	s_load_dwordx4 s[12:15], s[0:1], 0x0
	s_load_dwordx4 s[16:19], s[0:1], 0x10
	s_and_b32 s20, s2, 7
	s_lshr_b32 s21, s2, 3
	s_lshr_b32 s37, s20, 1
	s_and_b32 s36, s20, 1
	s_mul_i32 s36, s36, 31
	s_add_i32 s36, s36, s21
	s_lshr_b32 s21, s36, 1
	s_and_b32 s36, s36, 1
	s_lshl_b32 s37, s37, 1
	s_add_i32 s20, s37, s36
	v_lshrrev_b32_e32 v1, 6, v0
	v_and_b32_e32 v2, 63, v0
	s_nop 0
	v_readfirstlane_b32 s22, v1
	s_nop 3
	s_lshl_b32 s23, s20, 3
	s_add_i32 s23, s23, s22
	s_mul_i32 s24, s23, 0x439200
	s_mul_i32 s25, s21, 0x1f0
	s_add_u32 s24, s24, s25
	s_lshl_b32 s25, s21, 17
	s_lshl_b32 s26, s22, 13
	s_add_u32 s25, s25, s26
	s_mul_i32 s27, s20, 0x1e080
	s_mul_i32 s36, s21, 0x1f0
	s_add_u32 s27, s27, s36
	v_min_u32_e32 v10, 61, v2
	v_lshlrev_b32_e32 v3, 3, v10
	v_lshlrev_b32_e32 v4, 4, v2
	v_cmp_lt_u32_e32 vcc, 30, v10
	s_nop 1
	v_cndmask_b32_e64 v5, 0, 1, vcc
	v_mul_u32_u24_e32 v6, 31, v5
	v_sub_u32_e32 v6, v10, v6
	v_lshl_add_u32 v7, v1, 1, v5
	v_and_b32_e32 v8, 7, v6
	v_xor_b32_e32 v7, v7, v8
	v_lshlrev_b32_e32 v7, 4, v7
	v_lshl_add_u32 v5, v6, 12, v7
	s_lshl_b32 s36, s22, 2
	s_add_i32 s36, s36, 0
	s_and_b32 s36, s36, 7
	s_lshl_b32 s37, s22, 14
	s_add_i32 s37, s37, 0x0
	v_xor_b32_e32 v6, s36, v2
	v_lshlrev_b32_e32 v6, 4, v6
	v_add_u32_e32 v6, s37, v6
	s_lshl_b32 s36, s22, 2
	s_add_i32 s36, s36, 1
	s_and_b32 s36, s36, 7
	s_lshl_b32 s37, s22, 14
	s_add_i32 s37, s37, 0x1000
	v_xor_b32_e32 v7, s36, v2
	v_lshlrev_b32_e32 v7, 4, v7
	v_add_u32_e32 v7, s37, v7
	s_lshl_b32 s36, s22, 2
	s_add_i32 s36, s36, 2
	s_and_b32 s36, s36, 7
	s_lshl_b32 s37, s22, 14
	s_add_i32 s37, s37, 0x2000
	v_xor_b32_e32 v8, s36, v2
	v_lshlrev_b32_e32 v8, 4, v8
	v_add_u32_e32 v8, s37, v8
	s_lshl_b32 s36, s22, 2
	s_add_i32 s36, s36, 3
	s_and_b32 s36, s36, 7
	s_lshl_b32 s37, s22, 14
	s_add_i32 s37, s37, 0x3000
	v_xor_b32_e32 v9, s36, v2
	v_lshlrev_b32_e32 v9, 4, v9
	v_add_u32_e32 v9, s37, v9
	s_lshl_b32 s36, s22, 11
	s_add_i32 s36, s36, 0x20000
	v_add_u32_e32 v254, s36, v4
	s_add_i32 s37, s22, 1
	s_min_u32 s37, s37, 7
	s_lshl_b32 s37, s37, 11
	s_add_i32 s37, s37, 0x20000
	v_add_u32_e32 v255, s37, v4
	v_lshrrev_b32_e32 v10, 5, v0
	v_lshrrev_b32_e32 v11, 1, v10
	v_mul_u32_u24_e32 v11, 0x3c10, v11
	v_and_b32_e32 v10, 1, v10
	v_mul_u32_u24_e32 v10, 0xf8, v10
	v_add_u32_e32 v11, v11, v10
	v_and_b32_e32 v10, 31, v0
	v_lshl_add_u32 v11, v10, 3, v11
	v_add_u32_e32 v11, s27, v11
	v_cmp_eq_u32_e32 vcc, 31, v10
	v_mov_b32_e32 v10, 0x7f000000
	s_nop 1
	v_cndmask_b32_e32 v11, v11, v10, vcc
	s_waitcnt lgkmcnt(0)
	s_add_u32 s4, s12, s24
	s_addc_u32 s5, s13, 0
	s_and_b32 s5, s5, 0xffff
	s_sub_u32 s6, 0x10e48000, s24
	s_mov_b32 s7, 0x20000
	s_add_u32 s8, s14, s25
	s_addc_u32 s9, s15, 0
	s_and_b32 s9, s9, 0xffff
	s_sub_u32 s10, 0x400000, s25
	s_mov_b32 s11, 0x20000
	s_mov_b32 s28, s16
	s_and_b32 s29, s17, 0xffff
	s_mov_b32 s30, 0xf0400
	s_mov_b32 s31, 0x20000
	s_mov_b32 s32, s18
	s_and_b32 s33, s19, 0xffff
	s_mov_b32 s34, 0xf04000
	s_mov_b32 s35, 0x20000
	s_mov_b32 s40, 0x0
	s_mov_b32 s41, 0x21c90
	s_mov_b32 s42, 0x43920
	s_mov_b32 s43, 0x655b0
	s_mov_b32 s44, 0x87240
	s_mov_b32 s45, 0xa8ed0
	s_mov_b32 s46, 0xcab60
	s_mov_b32 s47, 0xec7f0
	buffer_load_dwordx2 v[44:45], v3, s[4:7], s40 offen nt
	buffer_load_dwordx2 v[46:47], v3, s[4:7], s41 offen nt
	buffer_load_dwordx2 v[48:49], v3, s[4:7], s42 offen nt
	buffer_load_dwordx2 v[50:51], v3, s[4:7], s43 offen nt
	buffer_load_dwordx2 v[52:53], v3, s[4:7], s44 offen nt
	buffer_load_dwordx2 v[54:55], v3, s[4:7], s45 offen nt
	buffer_load_dwordx2 v[56:57], v3, s[4:7], s46 offen nt
	buffer_load_dwordx2 v[58:59], v3, s[4:7], s47 offen nt
	s_mov_b32 s40, 0x10e480
	s_mov_b32 s41, 0x130110
	s_mov_b32 s42, 0x151da0
	s_mov_b32 s43, 0x173a30
	s_mov_b32 s44, 0x1956c0
	s_mov_b32 s45, 0x1b7350
	s_mov_b32 s46, 0x1d8fe0
	s_mov_b32 s47, 0x1fac70
	buffer_load_dwordx2 v[60:61], v3, s[4:7], s40 offen nt
	buffer_load_dwordx2 v[62:63], v3, s[4:7], s41 offen nt
	buffer_load_dwordx2 v[64:65], v3, s[4:7], s42 offen nt
	buffer_load_dwordx2 v[66:67], v3, s[4:7], s43 offen nt
	buffer_load_dwordx2 v[68:69], v3, s[4:7], s44 offen nt
	buffer_load_dwordx2 v[70:71], v3, s[4:7], s45 offen nt
	buffer_load_dwordx2 v[72:73], v3, s[4:7], s46 offen nt
	buffer_load_dwordx2 v[74:75], v3, s[4:7], s47 offen nt
	s_mov_b32 s40, 0x21c900
	s_mov_b32 s41, 0x23e590
	s_mov_b32 s42, 0x260220
	s_mov_b32 s43, 0x281eb0
	s_mov_b32 s44, 0x2a3b40
	s_mov_b32 s45, 0x2c57d0
	s_mov_b32 s46, 0x2e7460
	s_mov_b32 s47, 0x3090f0
	buffer_load_dwordx2 v[76:77], v3, s[4:7], s40 offen nt
	buffer_load_dwordx2 v[78:79], v3, s[4:7], s41 offen nt
	buffer_load_dwordx2 v[80:81], v3, s[4:7], s42 offen nt
	buffer_load_dwordx2 v[82:83], v3, s[4:7], s43 offen nt
	buffer_load_dwordx2 v[84:85], v3, s[4:7], s44 offen nt
	buffer_load_dwordx2 v[86:87], v3, s[4:7], s45 offen nt
	buffer_load_dwordx2 v[88:89], v3, s[4:7], s46 offen nt
	buffer_load_dwordx2 v[90:91], v3, s[4:7], s47 offen nt
	s_mov_b32 s40, 0x32ad80
	s_mov_b32 s41, 0x34ca10
	s_mov_b32 s42, 0x36e6a0
	s_mov_b32 s43, 0x390330
	s_mov_b32 s44, 0x3b1fc0
	s_mov_b32 s45, 0x3d3c50
	s_mov_b32 s46, 0x3f58e0
	s_mov_b32 s47, 0x417570
	buffer_load_dwordx2 v[92:93], v3, s[4:7], s40 offen nt
	buffer_load_dwordx2 v[94:95], v3, s[4:7], s41 offen nt
	buffer_load_dwordx2 v[96:97], v3, s[4:7], s42 offen nt
	buffer_load_dwordx2 v[98:99], v3, s[4:7], s43 offen nt
	buffer_load_dwordx2 v[100:101], v3, s[4:7], s44 offen nt
	buffer_load_dwordx2 v[102:103], v3, s[4:7], s45 offen nt
	buffer_load_dwordx2 v[104:105], v3, s[4:7], s46 offen nt
	buffer_load_dwordx2 v[106:107], v3, s[4:7], s47 offen nt
	buffer_load_dwordx2 v[252:253], v11, s[28:31], 0 offen
	s_mov_b32 s40, 0x0
	s_mov_b32 s41, 0x400
	s_mov_b32 s42, 0x800
	s_mov_b32 s43, 0xc00
	buffer_load_dwordx4 v[108:111], v4, s[8:11], s40 offen
	buffer_load_dwordx4 v[112:115], v4, s[8:11], s41 offen
	buffer_load_dwordx4 v[116:119], v4, s[8:11], s42 offen
	buffer_load_dwordx4 v[120:123], v4, s[8:11], s43 offen
	s_mov_b32 s40, 0x1000
	s_mov_b32 s41, 0x1400
	s_mov_b32 s42, 0x1800
	s_mov_b32 s43, 0x1c00
	buffer_load_dwordx4 v[124:127], v4, s[8:11], s40 offen
	buffer_load_dwordx4 v[128:131], v4, s[8:11], s41 offen
	buffer_load_dwordx4 v[132:135], v4, s[8:11], s42 offen
	buffer_load_dwordx4 v[136:139], v4, s[8:11], s43 offen
	s_mov_b32 s40, 0x10000
	s_mov_b32 s41, 0x10400
	s_mov_b32 s42, 0x10800
	s_mov_b32 s43, 0x10c00
	buffer_load_dwordx4 v[148:151], v4, s[8:11], s40 offen
	buffer_load_dwordx4 v[152:155], v4, s[8:11], s41 offen
	buffer_load_dwordx4 v[156:159], v4, s[8:11], s42 offen
	buffer_load_dwordx4 v[160:163], v4, s[8:11], s43 offen
	s_mov_b32 s40, 0x11000
	s_mov_b32 s41, 0x11400
	s_mov_b32 s42, 0x11800
	s_mov_b32 s43, 0x11c00
	buffer_load_dwordx4 v[164:167], v4, s[8:11], s40 offen
	buffer_load_dwordx4 v[168:171], v4, s[8:11], s41 offen
	buffer_load_dwordx4 v[172:175], v4, s[8:11], s42 offen
	buffer_load_dwordx4 v[176:179], v4, s[8:11], s43 offen
	s_waitcnt vmcnt(41)
	v_cvt_pkrtz_f16_f32 v12, v44, v46
	v_cvt_pkrtz_f16_f32 v13, v48, v50
	v_cvt_pkrtz_f16_f32 v14, v52, v54
	v_cvt_pkrtz_f16_f32 v15, v56, v58
	v_cvt_pkrtz_f16_f32 v16, v45, v47
	v_cvt_pkrtz_f16_f32 v17, v49, v51
	v_cvt_pkrtz_f16_f32 v18, v53, v55
	v_cvt_pkrtz_f16_f32 v19, v57, v59
	ds_write_b128 v5, v[12:15] offset:0
	ds_write_b128 v5, v[16:19] offset:2048
	s_waitcnt vmcnt(33)
	v_cvt_pkrtz_f16_f32 v12, v60, v62
	v_cvt_pkrtz_f16_f32 v13, v64, v66
	v_cvt_pkrtz_f16_f32 v14, v68, v70
	v_cvt_pkrtz_f16_f32 v15, v72, v74
	v_cvt_pkrtz_f16_f32 v16, v61, v63
	v_cvt_pkrtz_f16_f32 v17, v65, v67
	v_cvt_pkrtz_f16_f32 v18, v69, v71
	v_cvt_pkrtz_f16_f32 v19, v73, v75
	s_mov_b32 s40, 0x3c10
	s_mov_b32 s41, 0x258a0
	s_mov_b32 s42, 0x47530
	s_mov_b32 s43, 0x691c0
	s_mov_b32 s44, 0x8ae50
	s_mov_b32 s45, 0xacae0
	s_mov_b32 s46, 0xce770
	s_mov_b32 s47, 0xf0400
	buffer_load_dwordx2 v[44:45], v3, s[4:7], s40 offen nt
	buffer_load_dwordx2 v[46:47], v3, s[4:7], s41 offen nt
	buffer_load_dwordx2 v[48:49], v3, s[4:7], s42 offen nt
	buffer_load_dwordx2 v[50:51], v3, s[4:7], s43 offen nt
	buffer_load_dwordx2 v[52:53], v3, s[4:7], s44 offen nt
	buffer_load_dwordx2 v[54:55], v3, s[4:7], s45 offen nt
	buffer_load_dwordx2 v[56:57], v3, s[4:7], s46 offen nt
	buffer_load_dwordx2 v[58:59], v3, s[4:7], s47 offen nt
	ds_write_b128 v5, v[12:15] offset:256
	ds_write_b128 v5, v[16:19] offset:2304
	s_waitcnt vmcnt(33)
	v_cvt_pkrtz_f16_f32 v12, v76, v78
	v_cvt_pkrtz_f16_f32 v13, v80, v82
	v_cvt_pkrtz_f16_f32 v14, v84, v86
	v_cvt_pkrtz_f16_f32 v15, v88, v90
	v_cvt_pkrtz_f16_f32 v16, v77, v79
	v_cvt_pkrtz_f16_f32 v17, v81, v83
	v_cvt_pkrtz_f16_f32 v18, v85, v87
	v_cvt_pkrtz_f16_f32 v19, v89, v91
	s_mov_b32 s40, 0x112090
	s_mov_b32 s41, 0x133d20
	s_mov_b32 s42, 0x1559b0
	s_mov_b32 s43, 0x177640
	s_mov_b32 s44, 0x1992d0
	s_mov_b32 s45, 0x1baf60
	s_mov_b32 s46, 0x1dcbf0
	s_mov_b32 s47, 0x1fe880
	buffer_load_dwordx2 v[60:61], v3, s[4:7], s40 offen nt
	buffer_load_dwordx2 v[62:63], v3, s[4:7], s41 offen nt
	buffer_load_dwordx2 v[64:65], v3, s[4:7], s42 offen nt
	buffer_load_dwordx2 v[66:67], v3, s[4:7], s43 offen nt
	buffer_load_dwordx2 v[68:69], v3, s[4:7], s44 offen nt
	buffer_load_dwordx2 v[70:71], v3, s[4:7], s45 offen nt
	buffer_load_dwordx2 v[72:73], v3, s[4:7], s46 offen nt
	buffer_load_dwordx2 v[74:75], v3, s[4:7], s47 offen nt
	ds_write_b128 v5, v[12:15] offset:512
	ds_write_b128 v5, v[16:19] offset:2560
	s_waitcnt vmcnt(33)
	v_cvt_pkrtz_f16_f32 v12, v92, v94
	v_cvt_pkrtz_f16_f32 v13, v96, v98
	v_cvt_pkrtz_f16_f32 v14, v100, v102
	v_cvt_pkrtz_f16_f32 v15, v104, v106
	v_cvt_pkrtz_f16_f32 v16, v93, v95
	v_cvt_pkrtz_f16_f32 v17, v97, v99
	v_cvt_pkrtz_f16_f32 v18, v101, v103
	v_cvt_pkrtz_f16_f32 v19, v105, v107
	s_mov_b32 s40, 0x220510
	s_mov_b32 s41, 0x2421a0
	s_mov_b32 s42, 0x263e30
	s_mov_b32 s43, 0x285ac0
	s_mov_b32 s44, 0x2a7750
	s_mov_b32 s45, 0x2c93e0
	s_mov_b32 s46, 0x2eb070
	s_mov_b32 s47, 0x30cd00
	buffer_load_dwordx2 v[76:77], v3, s[4:7], s40 offen nt
	buffer_load_dwordx2 v[78:79], v3, s[4:7], s41 offen nt
	buffer_load_dwordx2 v[80:81], v3, s[4:7], s42 offen nt
	buffer_load_dwordx2 v[82:83], v3, s[4:7], s43 offen nt
	buffer_load_dwordx2 v[84:85], v3, s[4:7], s44 offen nt
	buffer_load_dwordx2 v[86:87], v3, s[4:7], s45 offen nt
	buffer_load_dwordx2 v[88:89], v3, s[4:7], s46 offen nt
	buffer_load_dwordx2 v[90:91], v3, s[4:7], s47 offen nt
	ds_write_b128 v5, v[12:15] offset:768
	ds_write_b128 v5, v[16:19] offset:2816
	s_waitcnt lgkmcnt(0)
	s_barrier
	s_waitcnt vmcnt(24)
	ds_write_b128 v254, v[108:111] offset:0
	ds_write_b128 v254, v[112:115] offset:1024
	ds_write_b128 v254, v[148:151] offset:16384
	ds_write_b128 v254, v[152:155] offset:17408
	s_waitcnt lgkmcnt(0)
	s_barrier
	ds_read_b128 v[140:143], v255 offset:0
	ds_read_b128 v[144:147], v255 offset:1024
	ds_read_b128 v[180:183], v255 offset:16384
	ds_read_b128 v[184:187], v255 offset:17408
	ds_read_b128 v[12:15], v6 offset:0
	ds_read_b128 v[16:19], v6 offset:2048
	ds_read_b128 v[20:23], v7 offset:0
	ds_read_b128 v[24:27], v7 offset:2048
	ds_read_b128 v[28:31], v8 offset:0
	ds_read_b128 v[32:35], v8 offset:2048
	ds_read_b128 v[36:39], v9 offset:0
	ds_read_b128 v[40:43], v9 offset:2048
	s_waitcnt lgkmcnt(7)
	v_mfma_f32_16x16x32_f16 v[188:191], v[108:111], v[12:15], 0
	v_mfma_f32_16x16x32_f16 v[220:223], v[148:151], v[12:15], 0
	s_waitcnt lgkmcnt(6)
	v_mfma_f32_16x16x32_f16 v[192:195], v[112:115], v[16:19], 0
	v_mfma_f32_16x16x32_f16 v[224:227], v[152:155], v[16:19], 0
	s_waitcnt lgkmcnt(5)
	v_mfma_f32_16x16x32_f16 v[196:199], v[116:119], v[20:23], 0
	v_mfma_f32_16x16x32_f16 v[228:231], v[156:159], v[20:23], 0
	s_waitcnt lgkmcnt(4)
	v_mfma_f32_16x16x32_f16 v[200:203], v[120:123], v[24:27], 0
	v_mfma_f32_16x16x32_f16 v[232:235], v[160:163], v[24:27], 0
	s_waitcnt lgkmcnt(3)
	v_mfma_f32_16x16x32_f16 v[204:207], v[124:127], v[28:31], 0
	v_mfma_f32_16x16x32_f16 v[236:239], v[164:167], v[28:31], 0
	s_waitcnt lgkmcnt(2)
	v_mfma_f32_16x16x32_f16 v[208:211], v[128:131], v[32:35], 0
	v_mfma_f32_16x16x32_f16 v[240:243], v[168:171], v[32:35], 0
	s_waitcnt lgkmcnt(1)
	v_mfma_f32_16x16x32_f16 v[212:215], v[132:135], v[36:39], 0
	v_mfma_f32_16x16x32_f16 v[244:247], v[172:175], v[36:39], 0
	s_waitcnt lgkmcnt(0)
	v_mfma_f32_16x16x32_f16 v[216:219], v[136:139], v[40:43], 0
	v_mfma_f32_16x16x32_f16 v[248:251], v[176:179], v[40:43], 0
	s_mov_b32 s40, 0x32e990
	s_mov_b32 s41, 0x350620
	s_mov_b32 s42, 0x3722b0
	s_mov_b32 s43, 0x393f40
	s_mov_b32 s44, 0x3b5bd0
	s_mov_b32 s45, 0x3d7860
	s_mov_b32 s46, 0x3f94f0
	s_mov_b32 s47, 0x41b180
	buffer_load_dwordx2 v[92:93], v3, s[4:7], s40 offen nt
	buffer_load_dwordx2 v[94:95], v3, s[4:7], s41 offen nt
	buffer_load_dwordx2 v[96:97], v3, s[4:7], s42 offen nt
	buffer_load_dwordx2 v[98:99], v3, s[4:7], s43 offen nt
	buffer_load_dwordx2 v[100:101], v3, s[4:7], s44 offen nt
	buffer_load_dwordx2 v[102:103], v3, s[4:7], s45 offen nt
	buffer_load_dwordx2 v[104:105], v3, s[4:7], s46 offen nt
	buffer_load_dwordx2 v[106:107], v3, s[4:7], s47 offen nt
	s_waitcnt vmcnt(24)
	v_cvt_pkrtz_f16_f32 v12, v44, v46
	v_cvt_pkrtz_f16_f32 v13, v48, v50
	v_cvt_pkrtz_f16_f32 v14, v52, v54
	v_cvt_pkrtz_f16_f32 v15, v56, v58
	v_cvt_pkrtz_f16_f32 v16, v45, v47
	v_cvt_pkrtz_f16_f32 v17, v49, v51
	v_cvt_pkrtz_f16_f32 v18, v53, v55
	v_cvt_pkrtz_f16_f32 v19, v57, v59
	ds_write_b128 v5, v[12:15] offset:1024
	ds_write_b128 v5, v[16:19] offset:3072
	s_waitcnt vmcnt(16)
	v_cvt_pkrtz_f16_f32 v12, v60, v62
	v_cvt_pkrtz_f16_f32 v13, v64, v66
	v_cvt_pkrtz_f16_f32 v14, v68, v70
	v_cvt_pkrtz_f16_f32 v15, v72, v74
	v_cvt_pkrtz_f16_f32 v16, v61, v63
	v_cvt_pkrtz_f16_f32 v17, v65, v67
	v_cvt_pkrtz_f16_f32 v18, v69, v71
	v_cvt_pkrtz_f16_f32 v19, v73, v75
	s_mov_b32 s40, 0x7820
	s_mov_b32 s41, 0x294b0
	s_mov_b32 s42, 0x4b140
	s_mov_b32 s43, 0x6cdd0
	s_mov_b32 s44, 0x8ea60
	s_mov_b32 s45, 0xb06f0
	s_mov_b32 s46, 0xd2380
	s_mov_b32 s47, 0xf4010
	buffer_load_dwordx2 v[44:45], v3, s[4:7], s40 offen nt
	buffer_load_dwordx2 v[46:47], v3, s[4:7], s41 offen nt
	buffer_load_dwordx2 v[48:49], v3, s[4:7], s42 offen nt
	buffer_load_dwordx2 v[50:51], v3, s[4:7], s43 offen nt
	buffer_load_dwordx2 v[52:53], v3, s[4:7], s44 offen nt
	buffer_load_dwordx2 v[54:55], v3, s[4:7], s45 offen nt
	buffer_load_dwordx2 v[56:57], v3, s[4:7], s46 offen nt
	buffer_load_dwordx2 v[58:59], v3, s[4:7], s47 offen nt
	ds_write_b128 v5, v[12:15] offset:1280
	ds_write_b128 v5, v[16:19] offset:3328
	s_waitcnt vmcnt(16)
	v_cvt_pkrtz_f16_f32 v12, v76, v78
	v_cvt_pkrtz_f16_f32 v13, v80, v82
	v_cvt_pkrtz_f16_f32 v14, v84, v86
	v_cvt_pkrtz_f16_f32 v15, v88, v90
	v_cvt_pkrtz_f16_f32 v16, v77, v79
	v_cvt_pkrtz_f16_f32 v17, v81, v83
	v_cvt_pkrtz_f16_f32 v18, v85, v87
	v_cvt_pkrtz_f16_f32 v19, v89, v91
	s_mov_b32 s40, 0x115ca0
	s_mov_b32 s41, 0x137930
	s_mov_b32 s42, 0x1595c0
	s_mov_b32 s43, 0x17b250
	s_mov_b32 s44, 0x19cee0
	s_mov_b32 s45, 0x1beb70
	s_mov_b32 s46, 0x1e0800
	s_mov_b32 s47, 0x202490
	buffer_load_dwordx2 v[60:61], v3, s[4:7], s40 offen nt
	buffer_load_dwordx2 v[62:63], v3, s[4:7], s41 offen nt
	buffer_load_dwordx2 v[64:65], v3, s[4:7], s42 offen nt
	buffer_load_dwordx2 v[66:67], v3, s[4:7], s43 offen nt
	buffer_load_dwordx2 v[68:69], v3, s[4:7], s44 offen nt
	buffer_load_dwordx2 v[70:71], v3, s[4:7], s45 offen nt
	buffer_load_dwordx2 v[72:73], v3, s[4:7], s46 offen nt
	buffer_load_dwordx2 v[74:75], v3, s[4:7], s47 offen nt
	ds_write_b128 v5, v[12:15] offset:1536
	ds_write_b128 v5, v[16:19] offset:3584
	s_waitcnt vmcnt(16)
	v_cvt_pkrtz_f16_f32 v12, v92, v94
	v_cvt_pkrtz_f16_f32 v13, v96, v98
	v_cvt_pkrtz_f16_f32 v14, v100, v102
	v_cvt_pkrtz_f16_f32 v15, v104, v106
	v_cvt_pkrtz_f16_f32 v16, v93, v95
	v_cvt_pkrtz_f16_f32 v17, v97, v99
	v_cvt_pkrtz_f16_f32 v18, v101, v103
	v_cvt_pkrtz_f16_f32 v19, v105, v107
	s_mov_b32 s40, 0x224120
	s_mov_b32 s41, 0x245db0
	s_mov_b32 s42, 0x267a40
	s_mov_b32 s43, 0x2896d0
	s_mov_b32 s44, 0x2ab360
	s_mov_b32 s45, 0x2ccff0
	s_mov_b32 s46, 0x2eec80
	s_mov_b32 s47, 0x310910
	buffer_load_dwordx2 v[76:77], v3, s[4:7], s40 offen nt
	buffer_load_dwordx2 v[78:79], v3, s[4:7], s41 offen nt
	buffer_load_dwordx2 v[80:81], v3, s[4:7], s42 offen nt
	buffer_load_dwordx2 v[82:83], v3, s[4:7], s43 offen nt
	buffer_load_dwordx2 v[84:85], v3, s[4:7], s44 offen nt
	buffer_load_dwordx2 v[86:87], v3, s[4:7], s45 offen nt
	buffer_load_dwordx2 v[88:89], v3, s[4:7], s46 offen nt
	buffer_load_dwordx2 v[90:91], v3, s[4:7], s47 offen nt
	ds_write_b128 v5, v[12:15] offset:1792
	ds_write_b128 v5, v[16:19] offset:3840
	s_waitcnt lgkmcnt(0)
	s_barrier
	ds_read_b128 v[12:15], v6 offset:1024
	ds_read_b128 v[16:19], v6 offset:3072
	ds_read_b128 v[20:23], v7 offset:1024
	ds_read_b128 v[24:27], v7 offset:3072
	ds_read_b128 v[28:31], v8 offset:1024
	ds_read_b128 v[32:35], v8 offset:3072
	ds_read_b128 v[36:39], v9 offset:1024
	ds_read_b128 v[40:43], v9 offset:3072
	s_waitcnt lgkmcnt(7)
	v_mfma_f32_16x16x32_f16 v[188:191], v[112:115], v[12:15], v[188:191]
	v_mfma_f32_16x16x32_f16 v[220:223], v[152:155], v[12:15], v[220:223]
	s_waitcnt lgkmcnt(6)
	v_mfma_f32_16x16x32_f16 v[192:195], v[116:119], v[16:19], v[192:195]
	v_mfma_f32_16x16x32_f16 v[224:227], v[156:159], v[16:19], v[224:227]
	s_waitcnt lgkmcnt(5)
	v_mfma_f32_16x16x32_f16 v[196:199], v[120:123], v[20:23], v[196:199]
	v_mfma_f32_16x16x32_f16 v[228:231], v[160:163], v[20:23], v[228:231]
	s_waitcnt lgkmcnt(4)
	v_mfma_f32_16x16x32_f16 v[200:203], v[124:127], v[24:27], v[200:203]
	v_mfma_f32_16x16x32_f16 v[232:235], v[164:167], v[24:27], v[232:235]
	s_waitcnt lgkmcnt(3)
	v_mfma_f32_16x16x32_f16 v[204:207], v[128:131], v[28:31], v[204:207]
	v_mfma_f32_16x16x32_f16 v[236:239], v[168:171], v[28:31], v[236:239]
	s_waitcnt lgkmcnt(2)
	v_mfma_f32_16x16x32_f16 v[208:211], v[132:135], v[32:35], v[208:211]
	v_mfma_f32_16x16x32_f16 v[240:243], v[172:175], v[32:35], v[240:243]
	s_waitcnt lgkmcnt(1)
	v_mfma_f32_16x16x32_f16 v[212:215], v[136:139], v[36:39], v[212:215]
	v_mfma_f32_16x16x32_f16 v[244:247], v[176:179], v[36:39], v[244:247]
	s_waitcnt lgkmcnt(0)
	v_mfma_f32_16x16x32_f16 v[216:219], v[140:143], v[40:43], v[216:219]
	v_mfma_f32_16x16x32_f16 v[248:251], v[180:183], v[40:43], v[248:251]
	s_mov_b32 s40, 0x3325a0
	s_mov_b32 s41, 0x354230
	s_mov_b32 s42, 0x375ec0
	s_mov_b32 s43, 0x397b50
	s_mov_b32 s44, 0x3b97e0
	s_mov_b32 s45, 0x3db470
	s_mov_b32 s46, 0x3fd100
	s_mov_b32 s47, 0x41ed90
	buffer_load_dwordx2 v[92:93], v3, s[4:7], s40 offen nt
	buffer_load_dwordx2 v[94:95], v3, s[4:7], s41 offen nt
	buffer_load_dwordx2 v[96:97], v3, s[4:7], s42 offen nt
	buffer_load_dwordx2 v[98:99], v3, s[4:7], s43 offen nt
	buffer_load_dwordx2 v[100:101], v3, s[4:7], s44 offen nt
	buffer_load_dwordx2 v[102:103], v3, s[4:7], s45 offen nt
	buffer_load_dwordx2 v[104:105], v3, s[4:7], s46 offen nt
	buffer_load_dwordx2 v[106:107], v3, s[4:7], s47 offen nt
	s_waitcnt vmcnt(24)
	v_cvt_pkrtz_f16_f32 v12, v44, v46
	v_cvt_pkrtz_f16_f32 v13, v48, v50
	v_cvt_pkrtz_f16_f32 v14, v52, v54
	v_cvt_pkrtz_f16_f32 v15, v56, v58
	v_cvt_pkrtz_f16_f32 v16, v45, v47
	v_cvt_pkrtz_f16_f32 v17, v49, v51
	v_cvt_pkrtz_f16_f32 v18, v53, v55
	v_cvt_pkrtz_f16_f32 v19, v57, v59
	ds_write_b128 v5, v[12:15] offset:0
	ds_write_b128 v5, v[16:19] offset:2048
	s_waitcnt vmcnt(16)
	v_cvt_pkrtz_f16_f32 v12, v60, v62
	v_cvt_pkrtz_f16_f32 v13, v64, v66
	v_cvt_pkrtz_f16_f32 v14, v68, v70
	v_cvt_pkrtz_f16_f32 v15, v72, v74
	v_cvt_pkrtz_f16_f32 v16, v61, v63
	v_cvt_pkrtz_f16_f32 v17, v65, v67
	v_cvt_pkrtz_f16_f32 v18, v69, v71
	v_cvt_pkrtz_f16_f32 v19, v73, v75
	s_mov_b32 s40, 0xb430
	s_mov_b32 s41, 0x2d0c0
	s_mov_b32 s42, 0x4ed50
	s_mov_b32 s43, 0x709e0
	s_mov_b32 s44, 0x92670
	s_mov_b32 s45, 0xb4300
	s_mov_b32 s46, 0xd5f90
	s_mov_b32 s47, 0xf7c20
	buffer_load_dwordx2 v[44:45], v3, s[4:7], s40 offen nt
	buffer_load_dwordx2 v[46:47], v3, s[4:7], s41 offen nt
	buffer_load_dwordx2 v[48:49], v3, s[4:7], s42 offen nt
	buffer_load_dwordx2 v[50:51], v3, s[4:7], s43 offen nt
	buffer_load_dwordx2 v[52:53], v3, s[4:7], s44 offen nt
	buffer_load_dwordx2 v[54:55], v3, s[4:7], s45 offen nt
	buffer_load_dwordx2 v[56:57], v3, s[4:7], s46 offen nt
	buffer_load_dwordx2 v[58:59], v3, s[4:7], s47 offen nt
	ds_write_b128 v5, v[12:15] offset:256
	ds_write_b128 v5, v[16:19] offset:2304
	s_waitcnt vmcnt(16)
	v_cvt_pkrtz_f16_f32 v12, v76, v78
	v_cvt_pkrtz_f16_f32 v13, v80, v82
	v_cvt_pkrtz_f16_f32 v14, v84, v86
	v_cvt_pkrtz_f16_f32 v15, v88, v90
	v_cvt_pkrtz_f16_f32 v16, v77, v79
	v_cvt_pkrtz_f16_f32 v17, v81, v83
	v_cvt_pkrtz_f16_f32 v18, v85, v87
	v_cvt_pkrtz_f16_f32 v19, v89, v91
	s_mov_b32 s40, 0x1198b0
	s_mov_b32 s41, 0x13b540
	s_mov_b32 s42, 0x15d1d0
	s_mov_b32 s43, 0x17ee60
	s_mov_b32 s44, 0x1a0af0
	s_mov_b32 s45, 0x1c2780
	s_mov_b32 s46, 0x1e4410
	s_mov_b32 s47, 0x2060a0
	buffer_load_dwordx2 v[60:61], v3, s[4:7], s40 offen nt
	buffer_load_dwordx2 v[62:63], v3, s[4:7], s41 offen nt
	buffer_load_dwordx2 v[64:65], v3, s[4:7], s42 offen nt
	buffer_load_dwordx2 v[66:67], v3, s[4:7], s43 offen nt
	buffer_load_dwordx2 v[68:69], v3, s[4:7], s44 offen nt
	buffer_load_dwordx2 v[70:71], v3, s[4:7], s45 offen nt
	buffer_load_dwordx2 v[72:73], v3, s[4:7], s46 offen nt
	buffer_load_dwordx2 v[74:75], v3, s[4:7], s47 offen nt
	ds_write_b128 v5, v[12:15] offset:512
	ds_write_b128 v5, v[16:19] offset:2560
	s_waitcnt vmcnt(16)
	v_cvt_pkrtz_f16_f32 v12, v92, v94
	v_cvt_pkrtz_f16_f32 v13, v96, v98
	v_cvt_pkrtz_f16_f32 v14, v100, v102
	v_cvt_pkrtz_f16_f32 v15, v104, v106
	v_cvt_pkrtz_f16_f32 v16, v93, v95
	v_cvt_pkrtz_f16_f32 v17, v97, v99
	v_cvt_pkrtz_f16_f32 v18, v101, v103
	v_cvt_pkrtz_f16_f32 v19, v105, v107
	s_mov_b32 s40, 0x227d30
	s_mov_b32 s41, 0x2499c0
	s_mov_b32 s42, 0x26b650
	s_mov_b32 s43, 0x28d2e0
	s_mov_b32 s44, 0x2aef70
	s_mov_b32 s45, 0x2d0c00
	s_mov_b32 s46, 0x2f2890
	s_mov_b32 s47, 0x314520
	buffer_load_dwordx2 v[76:77], v3, s[4:7], s40 offen nt
	buffer_load_dwordx2 v[78:79], v3, s[4:7], s41 offen nt
	buffer_load_dwordx2 v[80:81], v3, s[4:7], s42 offen nt
	buffer_load_dwordx2 v[82:83], v3, s[4:7], s43 offen nt
	buffer_load_dwordx2 v[84:85], v3, s[4:7], s44 offen nt
	buffer_load_dwordx2 v[86:87], v3, s[4:7], s45 offen nt
	buffer_load_dwordx2 v[88:89], v3, s[4:7], s46 offen nt
	buffer_load_dwordx2 v[90:91], v3, s[4:7], s47 offen nt
	ds_write_b128 v5, v[12:15] offset:768
	ds_write_b128 v5, v[16:19] offset:2816
	s_waitcnt lgkmcnt(0)
	s_barrier
	ds_read_b128 v[12:15], v6 offset:0
	ds_read_b128 v[16:19], v6 offset:2048
	ds_read_b128 v[20:23], v7 offset:0
	ds_read_b128 v[24:27], v7 offset:2048
	ds_read_b128 v[28:31], v8 offset:0
	ds_read_b128 v[32:35], v8 offset:2048
	ds_read_b128 v[36:39], v9 offset:0
	ds_read_b128 v[40:43], v9 offset:2048
	s_waitcnt lgkmcnt(7)
	v_mfma_f32_16x16x32_f16 v[188:191], v[116:119], v[12:15], v[188:191]
	v_mfma_f32_16x16x32_f16 v[220:223], v[156:159], v[12:15], v[220:223]
	s_waitcnt lgkmcnt(6)
	v_mfma_f32_16x16x32_f16 v[192:195], v[120:123], v[16:19], v[192:195]
	v_mfma_f32_16x16x32_f16 v[224:227], v[160:163], v[16:19], v[224:227]
	s_waitcnt lgkmcnt(5)
	v_mfma_f32_16x16x32_f16 v[196:199], v[124:127], v[20:23], v[196:199]
	v_mfma_f32_16x16x32_f16 v[228:231], v[164:167], v[20:23], v[228:231]
	s_waitcnt lgkmcnt(4)
	v_mfma_f32_16x16x32_f16 v[200:203], v[128:131], v[24:27], v[200:203]
	v_mfma_f32_16x16x32_f16 v[232:235], v[168:171], v[24:27], v[232:235]
	s_waitcnt lgkmcnt(3)
	v_mfma_f32_16x16x32_f16 v[204:207], v[132:135], v[28:31], v[204:207]
	v_mfma_f32_16x16x32_f16 v[236:239], v[172:175], v[28:31], v[236:239]
	s_waitcnt lgkmcnt(2)
	v_mfma_f32_16x16x32_f16 v[208:211], v[136:139], v[32:35], v[208:211]
	v_mfma_f32_16x16x32_f16 v[240:243], v[176:179], v[32:35], v[240:243]
	s_waitcnt lgkmcnt(1)
	v_mfma_f32_16x16x32_f16 v[212:215], v[140:143], v[36:39], v[212:215]
	v_mfma_f32_16x16x32_f16 v[244:247], v[180:183], v[36:39], v[244:247]
	s_waitcnt lgkmcnt(0)
	v_mfma_f32_16x16x32_f16 v[216:219], v[144:147], v[40:43], v[216:219]
	v_mfma_f32_16x16x32_f16 v[248:251], v[184:187], v[40:43], v[248:251]
	s_mov_b32 s40, 0x20000
	s_mov_b32 s41, 0x20400
	s_mov_b32 s42, 0x20800
	s_mov_b32 s43, 0x20c00
	buffer_load_dwordx4 v[108:111], v4, s[8:11], s40 offen
	buffer_load_dwordx4 v[112:115], v4, s[8:11], s41 offen
	buffer_load_dwordx4 v[116:119], v4, s[8:11], s42 offen
	buffer_load_dwordx4 v[120:123], v4, s[8:11], s43 offen
	s_mov_b32 s40, 0x21000
	s_mov_b32 s41, 0x21400
	s_mov_b32 s42, 0x21800
	s_mov_b32 s43, 0x21c00
	buffer_load_dwordx4 v[124:127], v4, s[8:11], s40 offen
	buffer_load_dwordx4 v[128:131], v4, s[8:11], s41 offen
	buffer_load_dwordx4 v[132:135], v4, s[8:11], s42 offen
	buffer_load_dwordx4 v[136:139], v4, s[8:11], s43 offen
	s_mov_b32 s40, 0x3361b0
	s_mov_b32 s41, 0x357e40
	s_mov_b32 s42, 0x379ad0
	s_mov_b32 s43, 0x39b760
	s_mov_b32 s44, 0x3bd3f0
	s_mov_b32 s45, 0x3df080
	s_mov_b32 s46, 0x400d10
	s_mov_b32 s47, 0x4229a0
	buffer_load_dwordx2 v[92:93], v3, s[4:7], s40 offen nt
	buffer_load_dwordx2 v[94:95], v3, s[4:7], s41 offen nt
	buffer_load_dwordx2 v[96:97], v3, s[4:7], s42 offen nt
	buffer_load_dwordx2 v[98:99], v3, s[4:7], s43 offen nt
	buffer_load_dwordx2 v[100:101], v3, s[4:7], s44 offen nt
	buffer_load_dwordx2 v[102:103], v3, s[4:7], s45 offen nt
	buffer_load_dwordx2 v[104:105], v3, s[4:7], s46 offen nt
	buffer_load_dwordx2 v[106:107], v3, s[4:7], s47 offen nt
	s_waitcnt vmcnt(32)
	v_cvt_pkrtz_f16_f32 v12, v44, v46
	v_cvt_pkrtz_f16_f32 v13, v48, v50
	v_cvt_pkrtz_f16_f32 v14, v52, v54
	v_cvt_pkrtz_f16_f32 v15, v56, v58
	v_cvt_pkrtz_f16_f32 v16, v45, v47
	v_cvt_pkrtz_f16_f32 v17, v49, v51
	v_cvt_pkrtz_f16_f32 v18, v53, v55
	v_cvt_pkrtz_f16_f32 v19, v57, v59
	ds_write_b128 v5, v[12:15] offset:1024
	ds_write_b128 v5, v[16:19] offset:3072
	s_waitcnt vmcnt(24)
	v_cvt_pkrtz_f16_f32 v12, v60, v62
	v_cvt_pkrtz_f16_f32 v13, v64, v66
	v_cvt_pkrtz_f16_f32 v14, v68, v70
	v_cvt_pkrtz_f16_f32 v15, v72, v74
	v_cvt_pkrtz_f16_f32 v16, v61, v63
	v_cvt_pkrtz_f16_f32 v17, v65, v67
	v_cvt_pkrtz_f16_f32 v18, v69, v71
	v_cvt_pkrtz_f16_f32 v19, v73, v75
	s_mov_b32 s40, 0xf040
	s_mov_b32 s41, 0x30cd0
	s_mov_b32 s42, 0x52960
	s_mov_b32 s43, 0x745f0
	s_mov_b32 s44, 0x96280
	s_mov_b32 s45, 0xb7f10
	s_mov_b32 s46, 0xd9ba0
	s_mov_b32 s47, 0xfb830
	buffer_load_dwordx2 v[44:45], v3, s[4:7], s40 offen nt
	buffer_load_dwordx2 v[46:47], v3, s[4:7], s41 offen nt
	buffer_load_dwordx2 v[48:49], v3, s[4:7], s42 offen nt
	buffer_load_dwordx2 v[50:51], v3, s[4:7], s43 offen nt
	buffer_load_dwordx2 v[52:53], v3, s[4:7], s44 offen nt
	buffer_load_dwordx2 v[54:55], v3, s[4:7], s45 offen nt
	buffer_load_dwordx2 v[56:57], v3, s[4:7], s46 offen nt
	buffer_load_dwordx2 v[58:59], v3, s[4:7], s47 offen nt
	ds_write_b128 v5, v[12:15] offset:1280
	ds_write_b128 v5, v[16:19] offset:3328
	s_waitcnt vmcnt(24)
	v_cvt_pkrtz_f16_f32 v12, v76, v78
	v_cvt_pkrtz_f16_f32 v13, v80, v82
	v_cvt_pkrtz_f16_f32 v14, v84, v86
	v_cvt_pkrtz_f16_f32 v15, v88, v90
	v_cvt_pkrtz_f16_f32 v16, v77, v79
	v_cvt_pkrtz_f16_f32 v17, v81, v83
	v_cvt_pkrtz_f16_f32 v18, v85, v87
	v_cvt_pkrtz_f16_f32 v19, v89, v91
	s_mov_b32 s40, 0x11d4c0
	s_mov_b32 s41, 0x13f150
	s_mov_b32 s42, 0x160de0
	s_mov_b32 s43, 0x182a70
	s_mov_b32 s44, 0x1a4700
	s_mov_b32 s45, 0x1c6390
	s_mov_b32 s46, 0x1e8020
	s_mov_b32 s47, 0x209cb0
	buffer_load_dwordx2 v[60:61], v3, s[4:7], s40 offen nt
	buffer_load_dwordx2 v[62:63], v3, s[4:7], s41 offen nt
	buffer_load_dwordx2 v[64:65], v3, s[4:7], s42 offen nt
	buffer_load_dwordx2 v[66:67], v3, s[4:7], s43 offen nt
	buffer_load_dwordx2 v[68:69], v3, s[4:7], s44 offen nt
	buffer_load_dwordx2 v[70:71], v3, s[4:7], s45 offen nt
	buffer_load_dwordx2 v[72:73], v3, s[4:7], s46 offen nt
	buffer_load_dwordx2 v[74:75], v3, s[4:7], s47 offen nt
	ds_write_b128 v5, v[12:15] offset:1536
	ds_write_b128 v5, v[16:19] offset:3584
	s_waitcnt vmcnt(16)
	v_cvt_pkrtz_f16_f32 v12, v92, v94
	v_cvt_pkrtz_f16_f32 v13, v96, v98
	v_cvt_pkrtz_f16_f32 v14, v100, v102
	v_cvt_pkrtz_f16_f32 v15, v104, v106
	v_cvt_pkrtz_f16_f32 v16, v93, v95
	v_cvt_pkrtz_f16_f32 v17, v97, v99
	v_cvt_pkrtz_f16_f32 v18, v101, v103
	v_cvt_pkrtz_f16_f32 v19, v105, v107
	s_mov_b32 s40, 0x22b940
	s_mov_b32 s41, 0x24d5d0
	s_mov_b32 s42, 0x26f260
	s_mov_b32 s43, 0x290ef0
	s_mov_b32 s44, 0x2b2b80
	s_mov_b32 s45, 0x2d4810
	s_mov_b32 s46, 0x2f64a0
	s_mov_b32 s47, 0x318130
	buffer_load_dwordx2 v[76:77], v3, s[4:7], s40 offen nt
	buffer_load_dwordx2 v[78:79], v3, s[4:7], s41 offen nt
	buffer_load_dwordx2 v[80:81], v3, s[4:7], s42 offen nt
	buffer_load_dwordx2 v[82:83], v3, s[4:7], s43 offen nt
	buffer_load_dwordx2 v[84:85], v3, s[4:7], s44 offen nt
	buffer_load_dwordx2 v[86:87], v3, s[4:7], s45 offen nt
	buffer_load_dwordx2 v[88:89], v3, s[4:7], s46 offen nt
	buffer_load_dwordx2 v[90:91], v3, s[4:7], s47 offen nt
	ds_write_b128 v5, v[12:15] offset:1792
	ds_write_b128 v5, v[16:19] offset:3840
	s_waitcnt lgkmcnt(0)
	s_barrier
	ds_write_b128 v254, v[108:111] offset:0
	ds_write_b128 v254, v[112:115] offset:1024
	s_waitcnt lgkmcnt(0)
	s_barrier
	ds_read_b128 v[140:143], v255 offset:0
	ds_read_b128 v[144:147], v255 offset:1024
	ds_read_b128 v[12:15], v6 offset:1024
	ds_read_b128 v[16:19], v6 offset:3072
	ds_read_b128 v[20:23], v7 offset:1024
	ds_read_b128 v[24:27], v7 offset:3072
	ds_read_b128 v[28:31], v8 offset:1024
	ds_read_b128 v[32:35], v8 offset:3072
	ds_read_b128 v[36:39], v9 offset:1024
	ds_read_b128 v[40:43], v9 offset:3072
	s_waitcnt lgkmcnt(7)
	v_mfma_f32_16x16x32_f16 v[188:191], v[148:151], v[12:15], v[188:191]
	v_mfma_f32_16x16x32_f16 v[220:223], v[108:111], v[12:15], v[220:223]
	s_waitcnt lgkmcnt(6)
	v_mfma_f32_16x16x32_f16 v[192:195], v[152:155], v[16:19], v[192:195]
	v_mfma_f32_16x16x32_f16 v[224:227], v[112:115], v[16:19], v[224:227]
	s_waitcnt lgkmcnt(5)
	v_mfma_f32_16x16x32_f16 v[196:199], v[156:159], v[20:23], v[196:199]
	v_mfma_f32_16x16x32_f16 v[228:231], v[116:119], v[20:23], v[228:231]
	s_waitcnt lgkmcnt(4)
	v_mfma_f32_16x16x32_f16 v[200:203], v[160:163], v[24:27], v[200:203]
	v_mfma_f32_16x16x32_f16 v[232:235], v[120:123], v[24:27], v[232:235]
	s_waitcnt lgkmcnt(3)
	v_mfma_f32_16x16x32_f16 v[204:207], v[164:167], v[28:31], v[204:207]
	v_mfma_f32_16x16x32_f16 v[236:239], v[124:127], v[28:31], v[236:239]
	s_waitcnt lgkmcnt(2)
	v_mfma_f32_16x16x32_f16 v[208:211], v[168:171], v[32:35], v[208:211]
	v_mfma_f32_16x16x32_f16 v[240:243], v[128:131], v[32:35], v[240:243]
	s_waitcnt lgkmcnt(1)
	v_mfma_f32_16x16x32_f16 v[212:215], v[172:175], v[36:39], v[212:215]
	v_mfma_f32_16x16x32_f16 v[244:247], v[132:135], v[36:39], v[244:247]
	s_waitcnt lgkmcnt(0)
	v_mfma_f32_16x16x32_f16 v[216:219], v[176:179], v[40:43], v[216:219]
	v_mfma_f32_16x16x32_f16 v[248:251], v[136:139], v[40:43], v[248:251]
	s_mov_b32 s40, 0x339dc0
	s_mov_b32 s41, 0x35ba50
	s_mov_b32 s42, 0x37d6e0
	s_mov_b32 s43, 0x39f370
	s_mov_b32 s44, 0x3c1000
	s_mov_b32 s45, 0x3e2c90
	s_mov_b32 s46, 0x404920
	s_mov_b32 s47, 0x4265b0
	buffer_load_dwordx2 v[92:93], v3, s[4:7], s40 offen nt
	buffer_load_dwordx2 v[94:95], v3, s[4:7], s41 offen nt
	buffer_load_dwordx2 v[96:97], v3, s[4:7], s42 offen nt
	buffer_load_dwordx2 v[98:99], v3, s[4:7], s43 offen nt
	buffer_load_dwordx2 v[100:101], v3, s[4:7], s44 offen nt
	buffer_load_dwordx2 v[102:103], v3, s[4:7], s45 offen nt
	buffer_load_dwordx2 v[104:105], v3, s[4:7], s46 offen nt
	buffer_load_dwordx2 v[106:107], v3, s[4:7], s47 offen nt
	s_waitcnt vmcnt(24)
	v_cvt_pkrtz_f16_f32 v12, v44, v46
	v_cvt_pkrtz_f16_f32 v13, v48, v50
	v_cvt_pkrtz_f16_f32 v14, v52, v54
	v_cvt_pkrtz_f16_f32 v15, v56, v58
	v_cvt_pkrtz_f16_f32 v16, v45, v47
	v_cvt_pkrtz_f16_f32 v17, v49, v51
	v_cvt_pkrtz_f16_f32 v18, v53, v55
	v_cvt_pkrtz_f16_f32 v19, v57, v59
	ds_write_b128 v5, v[12:15] offset:0
	ds_write_b128 v5, v[16:19] offset:2048
	s_waitcnt vmcnt(16)
	v_cvt_pkrtz_f16_f32 v12, v60, v62
	v_cvt_pkrtz_f16_f32 v13, v64, v66
	v_cvt_pkrtz_f16_f32 v14, v68, v70
	v_cvt_pkrtz_f16_f32 v15, v72, v74
	v_cvt_pkrtz_f16_f32 v16, v61, v63
	v_cvt_pkrtz_f16_f32 v17, v65, v67
	v_cvt_pkrtz_f16_f32 v18, v69, v71
	v_cvt_pkrtz_f16_f32 v19, v73, v75
	s_mov_b32 s40, 0x12c50
	s_mov_b32 s41, 0x348e0
	s_mov_b32 s42, 0x56570
	s_mov_b32 s43, 0x78200
	s_mov_b32 s44, 0x99e90
	s_mov_b32 s45, 0xbbb20
	s_mov_b32 s46, 0xdd7b0
	s_mov_b32 s47, 0xff440
	buffer_load_dwordx2 v[44:45], v3, s[4:7], s40 offen nt
	buffer_load_dwordx2 v[46:47], v3, s[4:7], s41 offen nt
	buffer_load_dwordx2 v[48:49], v3, s[4:7], s42 offen nt
	buffer_load_dwordx2 v[50:51], v3, s[4:7], s43 offen nt
	buffer_load_dwordx2 v[52:53], v3, s[4:7], s44 offen nt
	buffer_load_dwordx2 v[54:55], v3, s[4:7], s45 offen nt
	buffer_load_dwordx2 v[56:57], v3, s[4:7], s46 offen nt
	buffer_load_dwordx2 v[58:59], v3, s[4:7], s47 offen nt
	ds_write_b128 v5, v[12:15] offset:256
	ds_write_b128 v5, v[16:19] offset:2304
	s_waitcnt vmcnt(16)
	v_cvt_pkrtz_f16_f32 v12, v76, v78
	v_cvt_pkrtz_f16_f32 v13, v80, v82
	v_cvt_pkrtz_f16_f32 v14, v84, v86
	v_cvt_pkrtz_f16_f32 v15, v88, v90
	v_cvt_pkrtz_f16_f32 v16, v77, v79
	v_cvt_pkrtz_f16_f32 v17, v81, v83
	v_cvt_pkrtz_f16_f32 v18, v85, v87
	v_cvt_pkrtz_f16_f32 v19, v89, v91
	s_mov_b32 s40, 0x1210d0
	s_mov_b32 s41, 0x142d60
	s_mov_b32 s42, 0x1649f0
	s_mov_b32 s43, 0x186680
	s_mov_b32 s44, 0x1a8310
	s_mov_b32 s45, 0x1c9fa0
	s_mov_b32 s46, 0x1ebc30
	s_mov_b32 s47, 0x20d8c0
	buffer_load_dwordx2 v[60:61], v3, s[4:7], s40 offen nt
	buffer_load_dwordx2 v[62:63], v3, s[4:7], s41 offen nt
	buffer_load_dwordx2 v[64:65], v3, s[4:7], s42 offen nt
	buffer_load_dwordx2 v[66:67], v3, s[4:7], s43 offen nt
	buffer_load_dwordx2 v[68:69], v3, s[4:7], s44 offen nt
	buffer_load_dwordx2 v[70:71], v3, s[4:7], s45 offen nt
	buffer_load_dwordx2 v[72:73], v3, s[4:7], s46 offen nt
	buffer_load_dwordx2 v[74:75], v3, s[4:7], s47 offen nt
	ds_write_b128 v5, v[12:15] offset:512
	ds_write_b128 v5, v[16:19] offset:2560
	s_waitcnt vmcnt(16)
	v_cvt_pkrtz_f16_f32 v12, v92, v94
	v_cvt_pkrtz_f16_f32 v13, v96, v98
	v_cvt_pkrtz_f16_f32 v14, v100, v102
	v_cvt_pkrtz_f16_f32 v15, v104, v106
	v_cvt_pkrtz_f16_f32 v16, v93, v95
	v_cvt_pkrtz_f16_f32 v17, v97, v99
	v_cvt_pkrtz_f16_f32 v18, v101, v103
	v_cvt_pkrtz_f16_f32 v19, v105, v107
	s_mov_b32 s40, 0x22f550
	s_mov_b32 s41, 0x2511e0
	s_mov_b32 s42, 0x272e70
	s_mov_b32 s43, 0x294b00
	s_mov_b32 s44, 0x2b6790
	s_mov_b32 s45, 0x2d8420
	s_mov_b32 s46, 0x2fa0b0
	s_mov_b32 s47, 0x31bd40
	buffer_load_dwordx2 v[76:77], v3, s[4:7], s40 offen nt
	buffer_load_dwordx2 v[78:79], v3, s[4:7], s41 offen nt
	buffer_load_dwordx2 v[80:81], v3, s[4:7], s42 offen nt
	buffer_load_dwordx2 v[82:83], v3, s[4:7], s43 offen nt
	buffer_load_dwordx2 v[84:85], v3, s[4:7], s44 offen nt
	buffer_load_dwordx2 v[86:87], v3, s[4:7], s45 offen nt
	buffer_load_dwordx2 v[88:89], v3, s[4:7], s46 offen nt
	buffer_load_dwordx2 v[90:91], v3, s[4:7], s47 offen nt
	ds_write_b128 v5, v[12:15] offset:768
	ds_write_b128 v5, v[16:19] offset:2816
	s_waitcnt lgkmcnt(0)
	s_barrier
	ds_read_b128 v[12:15], v6 offset:0
	ds_read_b128 v[16:19], v6 offset:2048
	ds_read_b128 v[20:23], v7 offset:0
	ds_read_b128 v[24:27], v7 offset:2048
	ds_read_b128 v[28:31], v8 offset:0
	ds_read_b128 v[32:35], v8 offset:2048
	ds_read_b128 v[36:39], v9 offset:0
	ds_read_b128 v[40:43], v9 offset:2048
	s_waitcnt lgkmcnt(7)
	v_mfma_f32_16x16x32_f16 v[188:191], v[152:155], v[12:15], v[188:191]
	v_mfma_f32_16x16x32_f16 v[220:223], v[112:115], v[12:15], v[220:223]
	s_waitcnt lgkmcnt(6)
	v_mfma_f32_16x16x32_f16 v[192:195], v[156:159], v[16:19], v[192:195]
	v_mfma_f32_16x16x32_f16 v[224:227], v[116:119], v[16:19], v[224:227]
	s_waitcnt lgkmcnt(5)
	v_mfma_f32_16x16x32_f16 v[196:199], v[160:163], v[20:23], v[196:199]
	v_mfma_f32_16x16x32_f16 v[228:231], v[120:123], v[20:23], v[228:231]
	s_waitcnt lgkmcnt(4)
	v_mfma_f32_16x16x32_f16 v[200:203], v[164:167], v[24:27], v[200:203]
	v_mfma_f32_16x16x32_f16 v[232:235], v[124:127], v[24:27], v[232:235]
	s_waitcnt lgkmcnt(3)
	v_mfma_f32_16x16x32_f16 v[204:207], v[168:171], v[28:31], v[204:207]
	v_mfma_f32_16x16x32_f16 v[236:239], v[128:131], v[28:31], v[236:239]
	s_waitcnt lgkmcnt(2)
	v_mfma_f32_16x16x32_f16 v[208:211], v[172:175], v[32:35], v[208:211]
	v_mfma_f32_16x16x32_f16 v[240:243], v[132:135], v[32:35], v[240:243]
	s_waitcnt lgkmcnt(1)
	v_mfma_f32_16x16x32_f16 v[212:215], v[176:179], v[36:39], v[212:215]
	v_mfma_f32_16x16x32_f16 v[244:247], v[136:139], v[36:39], v[244:247]
	s_waitcnt lgkmcnt(0)
	v_mfma_f32_16x16x32_f16 v[216:219], v[180:183], v[40:43], v[216:219]
	v_mfma_f32_16x16x32_f16 v[248:251], v[140:143], v[40:43], v[248:251]
	s_mov_b32 s40, 0x33d9d0
	s_mov_b32 s41, 0x35f660
	s_mov_b32 s42, 0x3812f0
	s_mov_b32 s43, 0x3a2f80
	s_mov_b32 s44, 0x3c4c10
	s_mov_b32 s45, 0x3e68a0
	s_mov_b32 s46, 0x408530
	s_mov_b32 s47, 0x42a1c0
	buffer_load_dwordx2 v[92:93], v3, s[4:7], s40 offen nt
	buffer_load_dwordx2 v[94:95], v3, s[4:7], s41 offen nt
	buffer_load_dwordx2 v[96:97], v3, s[4:7], s42 offen nt
	buffer_load_dwordx2 v[98:99], v3, s[4:7], s43 offen nt
	buffer_load_dwordx2 v[100:101], v3, s[4:7], s44 offen nt
	buffer_load_dwordx2 v[102:103], v3, s[4:7], s45 offen nt
	buffer_load_dwordx2 v[104:105], v3, s[4:7], s46 offen nt
	buffer_load_dwordx2 v[106:107], v3, s[4:7], s47 offen nt
	s_waitcnt vmcnt(24)
	v_cvt_pkrtz_f16_f32 v12, v44, v46
	v_cvt_pkrtz_f16_f32 v13, v48, v50
	v_cvt_pkrtz_f16_f32 v14, v52, v54
	v_cvt_pkrtz_f16_f32 v15, v56, v58
	v_cvt_pkrtz_f16_f32 v16, v45, v47
	v_cvt_pkrtz_f16_f32 v17, v49, v51
	v_cvt_pkrtz_f16_f32 v18, v53, v55
	v_cvt_pkrtz_f16_f32 v19, v57, v59
	ds_write_b128 v5, v[12:15] offset:1024
	ds_write_b128 v5, v[16:19] offset:3072
	s_waitcnt vmcnt(16)
	v_cvt_pkrtz_f16_f32 v12, v60, v62
	v_cvt_pkrtz_f16_f32 v13, v64, v66
	v_cvt_pkrtz_f16_f32 v14, v68, v70
	v_cvt_pkrtz_f16_f32 v15, v72, v74
	v_cvt_pkrtz_f16_f32 v16, v61, v63
	v_cvt_pkrtz_f16_f32 v17, v65, v67
	v_cvt_pkrtz_f16_f32 v18, v69, v71
	v_cvt_pkrtz_f16_f32 v19, v73, v75
	s_mov_b32 s40, 0x16860
	s_mov_b32 s41, 0x384f0
	s_mov_b32 s42, 0x5a180
	s_mov_b32 s43, 0x7be10
	s_mov_b32 s44, 0x9daa0
	s_mov_b32 s45, 0xbf730
	s_mov_b32 s46, 0xe13c0
	s_mov_b32 s47, 0x103050
	buffer_load_dwordx2 v[44:45], v3, s[4:7], s40 offen nt
	buffer_load_dwordx2 v[46:47], v3, s[4:7], s41 offen nt
	buffer_load_dwordx2 v[48:49], v3, s[4:7], s42 offen nt
	buffer_load_dwordx2 v[50:51], v3, s[4:7], s43 offen nt
	buffer_load_dwordx2 v[52:53], v3, s[4:7], s44 offen nt
	buffer_load_dwordx2 v[54:55], v3, s[4:7], s45 offen nt
	buffer_load_dwordx2 v[56:57], v3, s[4:7], s46 offen nt
	buffer_load_dwordx2 v[58:59], v3, s[4:7], s47 offen nt
	ds_write_b128 v5, v[12:15] offset:1280
	ds_write_b128 v5, v[16:19] offset:3328
	s_waitcnt vmcnt(16)
	v_cvt_pkrtz_f16_f32 v12, v76, v78
	v_cvt_pkrtz_f16_f32 v13, v80, v82
	v_cvt_pkrtz_f16_f32 v14, v84, v86
	v_cvt_pkrtz_f16_f32 v15, v88, v90
	v_cvt_pkrtz_f16_f32 v16, v77, v79
	v_cvt_pkrtz_f16_f32 v17, v81, v83
	v_cvt_pkrtz_f16_f32 v18, v85, v87
	v_cvt_pkrtz_f16_f32 v19, v89, v91
	s_mov_b32 s40, 0x124ce0
	s_mov_b32 s41, 0x146970
	s_mov_b32 s42, 0x168600
	s_mov_b32 s43, 0x18a290
	s_mov_b32 s44, 0x1abf20
	s_mov_b32 s45, 0x1cdbb0
	s_mov_b32 s46, 0x1ef840
	s_mov_b32 s47, 0x2114d0
	buffer_load_dwordx2 v[60:61], v3, s[4:7], s40 offen nt
	buffer_load_dwordx2 v[62:63], v3, s[4:7], s41 offen nt
	buffer_load_dwordx2 v[64:65], v3, s[4:7], s42 offen nt
	buffer_load_dwordx2 v[66:67], v3, s[4:7], s43 offen nt
	buffer_load_dwordx2 v[68:69], v3, s[4:7], s44 offen nt
	buffer_load_dwordx2 v[70:71], v3, s[4:7], s45 offen nt
	buffer_load_dwordx2 v[72:73], v3, s[4:7], s46 offen nt
	buffer_load_dwordx2 v[74:75], v3, s[4:7], s47 offen nt
	ds_write_b128 v5, v[12:15] offset:1536
	ds_write_b128 v5, v[16:19] offset:3584
	s_waitcnt vmcnt(16)
	v_cvt_pkrtz_f16_f32 v12, v92, v94
	v_cvt_pkrtz_f16_f32 v13, v96, v98
	v_cvt_pkrtz_f16_f32 v14, v100, v102
	v_cvt_pkrtz_f16_f32 v15, v104, v106
	v_cvt_pkrtz_f16_f32 v16, v93, v95
	v_cvt_pkrtz_f16_f32 v17, v97, v99
	v_cvt_pkrtz_f16_f32 v18, v101, v103
	v_cvt_pkrtz_f16_f32 v19, v105, v107
	s_mov_b32 s40, 0x233160
	s_mov_b32 s41, 0x254df0
	s_mov_b32 s42, 0x276a80
	s_mov_b32 s43, 0x298710
	s_mov_b32 s44, 0x2ba3a0
	s_mov_b32 s45, 0x2dc030
	s_mov_b32 s46, 0x2fdcc0
	s_mov_b32 s47, 0x31f950
	buffer_load_dwordx2 v[76:77], v3, s[4:7], s40 offen nt
	buffer_load_dwordx2 v[78:79], v3, s[4:7], s41 offen nt
	buffer_load_dwordx2 v[80:81], v3, s[4:7], s42 offen nt
	buffer_load_dwordx2 v[82:83], v3, s[4:7], s43 offen nt
	buffer_load_dwordx2 v[84:85], v3, s[4:7], s44 offen nt
	buffer_load_dwordx2 v[86:87], v3, s[4:7], s45 offen nt
	buffer_load_dwordx2 v[88:89], v3, s[4:7], s46 offen nt
	buffer_load_dwordx2 v[90:91], v3, s[4:7], s47 offen nt
	ds_write_b128 v5, v[12:15] offset:1792
	ds_write_b128 v5, v[16:19] offset:3840
	s_waitcnt lgkmcnt(0)
	s_barrier
	ds_read_b128 v[12:15], v6 offset:1024
	ds_read_b128 v[16:19], v6 offset:3072
	ds_read_b128 v[20:23], v7 offset:1024
	ds_read_b128 v[24:27], v7 offset:3072
	ds_read_b128 v[28:31], v8 offset:1024
	ds_read_b128 v[32:35], v8 offset:3072
	ds_read_b128 v[36:39], v9 offset:1024
	ds_read_b128 v[40:43], v9 offset:3072
	s_waitcnt lgkmcnt(7)
	v_mfma_f32_16x16x32_f16 v[188:191], v[156:159], v[12:15], v[188:191]
	v_mfma_f32_16x16x32_f16 v[220:223], v[116:119], v[12:15], v[220:223]
	s_waitcnt lgkmcnt(6)
	v_mfma_f32_16x16x32_f16 v[192:195], v[160:163], v[16:19], v[192:195]
	v_mfma_f32_16x16x32_f16 v[224:227], v[120:123], v[16:19], v[224:227]
	s_waitcnt lgkmcnt(5)
	v_mfma_f32_16x16x32_f16 v[196:199], v[164:167], v[20:23], v[196:199]
	v_mfma_f32_16x16x32_f16 v[228:231], v[124:127], v[20:23], v[228:231]
	s_waitcnt lgkmcnt(4)
	v_mfma_f32_16x16x32_f16 v[200:203], v[168:171], v[24:27], v[200:203]
	v_mfma_f32_16x16x32_f16 v[232:235], v[128:131], v[24:27], v[232:235]
	s_waitcnt lgkmcnt(3)
	v_mfma_f32_16x16x32_f16 v[204:207], v[172:175], v[28:31], v[204:207]
	v_mfma_f32_16x16x32_f16 v[236:239], v[132:135], v[28:31], v[236:239]
	s_waitcnt lgkmcnt(2)
	v_mfma_f32_16x16x32_f16 v[208:211], v[176:179], v[32:35], v[208:211]
	v_mfma_f32_16x16x32_f16 v[240:243], v[136:139], v[32:35], v[240:243]
	s_waitcnt lgkmcnt(1)
	v_mfma_f32_16x16x32_f16 v[212:215], v[180:183], v[36:39], v[212:215]
	v_mfma_f32_16x16x32_f16 v[244:247], v[140:143], v[36:39], v[244:247]
	s_waitcnt lgkmcnt(0)
	v_mfma_f32_16x16x32_f16 v[216:219], v[184:187], v[40:43], v[216:219]
	v_mfma_f32_16x16x32_f16 v[248:251], v[144:147], v[40:43], v[248:251]
	s_mov_b32 s40, 0x30000
	s_mov_b32 s41, 0x30400
	s_mov_b32 s42, 0x30800
	s_mov_b32 s43, 0x30c00
	buffer_load_dwordx4 v[148:151], v4, s[8:11], s40 offen
	buffer_load_dwordx4 v[152:155], v4, s[8:11], s41 offen
	buffer_load_dwordx4 v[156:159], v4, s[8:11], s42 offen
	buffer_load_dwordx4 v[160:163], v4, s[8:11], s43 offen
	s_mov_b32 s40, 0x31000
	s_mov_b32 s41, 0x31400
	s_mov_b32 s42, 0x31800
	s_mov_b32 s43, 0x31c00
	buffer_load_dwordx4 v[164:167], v4, s[8:11], s40 offen
	buffer_load_dwordx4 v[168:171], v4, s[8:11], s41 offen
	buffer_load_dwordx4 v[172:175], v4, s[8:11], s42 offen
	buffer_load_dwordx4 v[176:179], v4, s[8:11], s43 offen
	s_mov_b32 s40, 0x3415e0
	s_mov_b32 s41, 0x363270
	s_mov_b32 s42, 0x384f00
	s_mov_b32 s43, 0x3a6b90
	s_mov_b32 s44, 0x3c8820
	s_mov_b32 s45, 0x3ea4b0
	s_mov_b32 s46, 0x40c140
	s_mov_b32 s47, 0x42ddd0
	buffer_load_dwordx2 v[92:93], v3, s[4:7], s40 offen nt
	buffer_load_dwordx2 v[94:95], v3, s[4:7], s41 offen nt
	buffer_load_dwordx2 v[96:97], v3, s[4:7], s42 offen nt
	buffer_load_dwordx2 v[98:99], v3, s[4:7], s43 offen nt
	buffer_load_dwordx2 v[100:101], v3, s[4:7], s44 offen nt
	buffer_load_dwordx2 v[102:103], v3, s[4:7], s45 offen nt
	buffer_load_dwordx2 v[104:105], v3, s[4:7], s46 offen nt
	buffer_load_dwordx2 v[106:107], v3, s[4:7], s47 offen nt
	s_waitcnt vmcnt(32)
	v_cvt_pkrtz_f16_f32 v12, v44, v46
	v_cvt_pkrtz_f16_f32 v13, v48, v50
	v_cvt_pkrtz_f16_f32 v14, v52, v54
	v_cvt_pkrtz_f16_f32 v15, v56, v58
	v_cvt_pkrtz_f16_f32 v16, v45, v47
	v_cvt_pkrtz_f16_f32 v17, v49, v51
	v_cvt_pkrtz_f16_f32 v18, v53, v55
	v_cvt_pkrtz_f16_f32 v19, v57, v59
	ds_write_b128 v5, v[12:15] offset:0
	ds_write_b128 v5, v[16:19] offset:2048
	s_waitcnt vmcnt(24)
	v_cvt_pkrtz_f16_f32 v12, v60, v62
	v_cvt_pkrtz_f16_f32 v13, v64, v66
	v_cvt_pkrtz_f16_f32 v14, v68, v70
	v_cvt_pkrtz_f16_f32 v15, v72, v74
	v_cvt_pkrtz_f16_f32 v16, v61, v63
	v_cvt_pkrtz_f16_f32 v17, v65, v67
	v_cvt_pkrtz_f16_f32 v18, v69, v71
	v_cvt_pkrtz_f16_f32 v19, v73, v75
	s_mov_b32 s40, 0x1a470
	s_mov_b32 s41, 0x3c100
	s_mov_b32 s42, 0x5dd90
	s_mov_b32 s43, 0x7fa20
	s_mov_b32 s44, 0xa16b0
	s_mov_b32 s45, 0xc3340
	s_mov_b32 s46, 0xe4fd0
	s_mov_b32 s47, 0x106c60
	buffer_load_dwordx2 v[44:45], v3, s[4:7], s40 offen nt
	buffer_load_dwordx2 v[46:47], v3, s[4:7], s41 offen nt
	buffer_load_dwordx2 v[48:49], v3, s[4:7], s42 offen nt
	buffer_load_dwordx2 v[50:51], v3, s[4:7], s43 offen nt
	buffer_load_dwordx2 v[52:53], v3, s[4:7], s44 offen nt
	buffer_load_dwordx2 v[54:55], v3, s[4:7], s45 offen nt
	buffer_load_dwordx2 v[56:57], v3, s[4:7], s46 offen nt
	buffer_load_dwordx2 v[58:59], v3, s[4:7], s47 offen nt
	ds_write_b128 v5, v[12:15] offset:256
	ds_write_b128 v5, v[16:19] offset:2304
	s_waitcnt vmcnt(24)
	v_cvt_pkrtz_f16_f32 v12, v76, v78
	v_cvt_pkrtz_f16_f32 v13, v80, v82
	v_cvt_pkrtz_f16_f32 v14, v84, v86
	v_cvt_pkrtz_f16_f32 v15, v88, v90
	v_cvt_pkrtz_f16_f32 v16, v77, v79
	v_cvt_pkrtz_f16_f32 v17, v81, v83
	v_cvt_pkrtz_f16_f32 v18, v85, v87
	v_cvt_pkrtz_f16_f32 v19, v89, v91
	s_mov_b32 s40, 0x1288f0
	s_mov_b32 s41, 0x14a580
	s_mov_b32 s42, 0x16c210
	s_mov_b32 s43, 0x18dea0
	s_mov_b32 s44, 0x1afb30
	s_mov_b32 s45, 0x1d17c0
	s_mov_b32 s46, 0x1f3450
	s_mov_b32 s47, 0x2150e0
	buffer_load_dwordx2 v[60:61], v3, s[4:7], s40 offen nt
	buffer_load_dwordx2 v[62:63], v3, s[4:7], s41 offen nt
	buffer_load_dwordx2 v[64:65], v3, s[4:7], s42 offen nt
	buffer_load_dwordx2 v[66:67], v3, s[4:7], s43 offen nt
	buffer_load_dwordx2 v[68:69], v3, s[4:7], s44 offen nt
	buffer_load_dwordx2 v[70:71], v3, s[4:7], s45 offen nt
	buffer_load_dwordx2 v[72:73], v3, s[4:7], s46 offen nt
	buffer_load_dwordx2 v[74:75], v3, s[4:7], s47 offen nt
	ds_write_b128 v5, v[12:15] offset:512
	ds_write_b128 v5, v[16:19] offset:2560
	s_waitcnt vmcnt(16)
	v_cvt_pkrtz_f16_f32 v12, v92, v94
	v_cvt_pkrtz_f16_f32 v13, v96, v98
	v_cvt_pkrtz_f16_f32 v14, v100, v102
	v_cvt_pkrtz_f16_f32 v15, v104, v106
	v_cvt_pkrtz_f16_f32 v16, v93, v95
	v_cvt_pkrtz_f16_f32 v17, v97, v99
	v_cvt_pkrtz_f16_f32 v18, v101, v103
	v_cvt_pkrtz_f16_f32 v19, v105, v107
	s_mov_b32 s40, 0x236d70
	s_mov_b32 s41, 0x258a00
	s_mov_b32 s42, 0x27a690
	s_mov_b32 s43, 0x29c320
	s_mov_b32 s44, 0x2bdfb0
	s_mov_b32 s45, 0x2dfc40
	s_mov_b32 s46, 0x3018d0
	s_mov_b32 s47, 0x323560
	buffer_load_dwordx2 v[76:77], v3, s[4:7], s40 offen nt
	buffer_load_dwordx2 v[78:79], v3, s[4:7], s41 offen nt
	buffer_load_dwordx2 v[80:81], v3, s[4:7], s42 offen nt
	buffer_load_dwordx2 v[82:83], v3, s[4:7], s43 offen nt
	buffer_load_dwordx2 v[84:85], v3, s[4:7], s44 offen nt
	buffer_load_dwordx2 v[86:87], v3, s[4:7], s45 offen nt
	buffer_load_dwordx2 v[88:89], v3, s[4:7], s46 offen nt
	buffer_load_dwordx2 v[90:91], v3, s[4:7], s47 offen nt
	ds_write_b128 v5, v[12:15] offset:768
	ds_write_b128 v5, v[16:19] offset:2816
	s_waitcnt lgkmcnt(0)
	s_barrier
	ds_write_b128 v254, v[148:151] offset:16384
	ds_write_b128 v254, v[152:155] offset:17408
	s_waitcnt lgkmcnt(0)
	s_barrier
	ds_read_b128 v[180:183], v255 offset:16384
	ds_read_b128 v[184:187], v255 offset:17408
	ds_read_b128 v[12:15], v6 offset:0
	ds_read_b128 v[16:19], v6 offset:2048
	ds_read_b128 v[20:23], v7 offset:0
	ds_read_b128 v[24:27], v7 offset:2048
	ds_read_b128 v[28:31], v8 offset:0
	ds_read_b128 v[32:35], v8 offset:2048
	ds_read_b128 v[36:39], v9 offset:0
	ds_read_b128 v[40:43], v9 offset:2048
	s_waitcnt lgkmcnt(7)
	v_mfma_f32_16x16x32_f16 v[188:191], v[108:111], v[12:15], v[188:191]
	v_mfma_f32_16x16x32_f16 v[220:223], v[148:151], v[12:15], v[220:223]
	s_waitcnt lgkmcnt(6)
	v_mfma_f32_16x16x32_f16 v[192:195], v[112:115], v[16:19], v[192:195]
	v_mfma_f32_16x16x32_f16 v[224:227], v[152:155], v[16:19], v[224:227]
	s_waitcnt lgkmcnt(5)
	v_mfma_f32_16x16x32_f16 v[196:199], v[116:119], v[20:23], v[196:199]
	v_mfma_f32_16x16x32_f16 v[228:231], v[156:159], v[20:23], v[228:231]
	s_waitcnt lgkmcnt(4)
	v_mfma_f32_16x16x32_f16 v[200:203], v[120:123], v[24:27], v[200:203]
	v_mfma_f32_16x16x32_f16 v[232:235], v[160:163], v[24:27], v[232:235]
	s_waitcnt lgkmcnt(3)
	v_mfma_f32_16x16x32_f16 v[204:207], v[124:127], v[28:31], v[204:207]
	v_mfma_f32_16x16x32_f16 v[236:239], v[164:167], v[28:31], v[236:239]
	s_waitcnt lgkmcnt(2)
	v_mfma_f32_16x16x32_f16 v[208:211], v[128:131], v[32:35], v[208:211]
	v_mfma_f32_16x16x32_f16 v[240:243], v[168:171], v[32:35], v[240:243]
	s_waitcnt lgkmcnt(1)
	v_mfma_f32_16x16x32_f16 v[212:215], v[132:135], v[36:39], v[212:215]
	v_mfma_f32_16x16x32_f16 v[244:247], v[172:175], v[36:39], v[244:247]
	s_waitcnt lgkmcnt(0)
	v_mfma_f32_16x16x32_f16 v[216:219], v[136:139], v[40:43], v[216:219]
	v_mfma_f32_16x16x32_f16 v[248:251], v[176:179], v[40:43], v[248:251]
	s_mov_b32 s40, 0x3451f0
	s_mov_b32 s41, 0x366e80
	s_mov_b32 s42, 0x388b10
	s_mov_b32 s43, 0x3aa7a0
	s_mov_b32 s44, 0x3cc430
	s_mov_b32 s45, 0x3ee0c0
	s_mov_b32 s46, 0x40fd50
	s_mov_b32 s47, 0x4319e0
	buffer_load_dwordx2 v[92:93], v3, s[4:7], s40 offen nt
	buffer_load_dwordx2 v[94:95], v3, s[4:7], s41 offen nt
	buffer_load_dwordx2 v[96:97], v3, s[4:7], s42 offen nt
	buffer_load_dwordx2 v[98:99], v3, s[4:7], s43 offen nt
	buffer_load_dwordx2 v[100:101], v3, s[4:7], s44 offen nt
	buffer_load_dwordx2 v[102:103], v3, s[4:7], s45 offen nt
	buffer_load_dwordx2 v[104:105], v3, s[4:7], s46 offen nt
	buffer_load_dwordx2 v[106:107], v3, s[4:7], s47 offen nt
	s_waitcnt vmcnt(24)
	v_cvt_pkrtz_f16_f32 v12, v44, v46
	v_cvt_pkrtz_f16_f32 v13, v48, v50
	v_cvt_pkrtz_f16_f32 v14, v52, v54
	v_cvt_pkrtz_f16_f32 v15, v56, v58
	v_cvt_pkrtz_f16_f32 v16, v45, v47
	v_cvt_pkrtz_f16_f32 v17, v49, v51
	v_cvt_pkrtz_f16_f32 v18, v53, v55
	v_cvt_pkrtz_f16_f32 v19, v57, v59
	ds_write_b128 v5, v[12:15] offset:1024
	ds_write_b128 v5, v[16:19] offset:3072
	s_waitcnt vmcnt(16)
	v_cvt_pkrtz_f16_f32 v12, v60, v62
	v_cvt_pkrtz_f16_f32 v13, v64, v66
	v_cvt_pkrtz_f16_f32 v14, v68, v70
	v_cvt_pkrtz_f16_f32 v15, v72, v74
	v_cvt_pkrtz_f16_f32 v16, v61, v63
	v_cvt_pkrtz_f16_f32 v17, v65, v67
	v_cvt_pkrtz_f16_f32 v18, v69, v71
	v_cvt_pkrtz_f16_f32 v19, v73, v75
	s_mov_b32 s40, 0x1e080
	s_mov_b32 s41, 0x3fd10
	s_mov_b32 s42, 0x619a0
	s_mov_b32 s43, 0x83630
	s_mov_b32 s44, 0xa52c0
	s_mov_b32 s45, 0xc6f50
	s_mov_b32 s46, 0xe8be0
	s_mov_b32 s47, 0x10a870
	buffer_load_dwordx2 v[44:45], v3, s[4:7], s40 offen nt
	buffer_load_dwordx2 v[46:47], v3, s[4:7], s41 offen nt
	buffer_load_dwordx2 v[48:49], v3, s[4:7], s42 offen nt
	buffer_load_dwordx2 v[50:51], v3, s[4:7], s43 offen nt
	buffer_load_dwordx2 v[52:53], v3, s[4:7], s44 offen nt
	buffer_load_dwordx2 v[54:55], v3, s[4:7], s45 offen nt
	buffer_load_dwordx2 v[56:57], v3, s[4:7], s46 offen nt
	buffer_load_dwordx2 v[58:59], v3, s[4:7], s47 offen nt
	ds_write_b128 v5, v[12:15] offset:1280
	ds_write_b128 v5, v[16:19] offset:3328
	s_waitcnt vmcnt(16)
	v_cvt_pkrtz_f16_f32 v12, v76, v78
	v_cvt_pkrtz_f16_f32 v13, v80, v82
	v_cvt_pkrtz_f16_f32 v14, v84, v86
	v_cvt_pkrtz_f16_f32 v15, v88, v90
	v_cvt_pkrtz_f16_f32 v16, v77, v79
	v_cvt_pkrtz_f16_f32 v17, v81, v83
	v_cvt_pkrtz_f16_f32 v18, v85, v87
	v_cvt_pkrtz_f16_f32 v19, v89, v91
	s_mov_b32 s40, 0x12c500
	s_mov_b32 s41, 0x14e190
	s_mov_b32 s42, 0x16fe20
	s_mov_b32 s43, 0x191ab0
	s_mov_b32 s44, 0x1b3740
	s_mov_b32 s45, 0x1d53d0
	s_mov_b32 s46, 0x1f7060
	s_mov_b32 s47, 0x218cf0
	buffer_load_dwordx2 v[60:61], v3, s[4:7], s40 offen nt
	buffer_load_dwordx2 v[62:63], v3, s[4:7], s41 offen nt
	buffer_load_dwordx2 v[64:65], v3, s[4:7], s42 offen nt
	buffer_load_dwordx2 v[66:67], v3, s[4:7], s43 offen nt
	buffer_load_dwordx2 v[68:69], v3, s[4:7], s44 offen nt
	buffer_load_dwordx2 v[70:71], v3, s[4:7], s45 offen nt
	buffer_load_dwordx2 v[72:73], v3, s[4:7], s46 offen nt
	buffer_load_dwordx2 v[74:75], v3, s[4:7], s47 offen nt
	ds_write_b128 v5, v[12:15] offset:1536
	ds_write_b128 v5, v[16:19] offset:3584
	s_waitcnt vmcnt(16)
	v_cvt_pkrtz_f16_f32 v12, v92, v94
	v_cvt_pkrtz_f16_f32 v13, v96, v98
	v_cvt_pkrtz_f16_f32 v14, v100, v102
	v_cvt_pkrtz_f16_f32 v15, v104, v106
	v_cvt_pkrtz_f16_f32 v16, v93, v95
	v_cvt_pkrtz_f16_f32 v17, v97, v99
	v_cvt_pkrtz_f16_f32 v18, v101, v103
	v_cvt_pkrtz_f16_f32 v19, v105, v107
	s_mov_b32 s40, 0x23a980
	s_mov_b32 s41, 0x25c610
	s_mov_b32 s42, 0x27e2a0
	s_mov_b32 s43, 0x29ff30
	s_mov_b32 s44, 0x2c1bc0
	s_mov_b32 s45, 0x2e3850
	s_mov_b32 s46, 0x3054e0
	s_mov_b32 s47, 0x327170
	buffer_load_dwordx2 v[76:77], v3, s[4:7], s40 offen nt
	buffer_load_dwordx2 v[78:79], v3, s[4:7], s41 offen nt
	buffer_load_dwordx2 v[80:81], v3, s[4:7], s42 offen nt
	buffer_load_dwordx2 v[82:83], v3, s[4:7], s43 offen nt
	buffer_load_dwordx2 v[84:85], v3, s[4:7], s44 offen nt
	buffer_load_dwordx2 v[86:87], v3, s[4:7], s45 offen nt
	buffer_load_dwordx2 v[88:89], v3, s[4:7], s46 offen nt
	buffer_load_dwordx2 v[90:91], v3, s[4:7], s47 offen nt
	ds_write_b128 v5, v[12:15] offset:1792
	ds_write_b128 v5, v[16:19] offset:3840
	s_waitcnt lgkmcnt(0)
	s_barrier
	ds_read_b128 v[12:15], v6 offset:1024
	ds_read_b128 v[16:19], v6 offset:3072
	ds_read_b128 v[20:23], v7 offset:1024
	ds_read_b128 v[24:27], v7 offset:3072
	ds_read_b128 v[28:31], v8 offset:1024
	ds_read_b128 v[32:35], v8 offset:3072
	ds_read_b128 v[36:39], v9 offset:1024
	ds_read_b128 v[40:43], v9 offset:3072
	s_waitcnt lgkmcnt(7)
	v_mfma_f32_16x16x32_f16 v[188:191], v[112:115], v[12:15], v[188:191]
	v_mfma_f32_16x16x32_f16 v[220:223], v[152:155], v[12:15], v[220:223]
	s_waitcnt lgkmcnt(6)
	v_mfma_f32_16x16x32_f16 v[192:195], v[116:119], v[16:19], v[192:195]
	v_mfma_f32_16x16x32_f16 v[224:227], v[156:159], v[16:19], v[224:227]
	s_waitcnt lgkmcnt(5)
	v_mfma_f32_16x16x32_f16 v[196:199], v[120:123], v[20:23], v[196:199]
	v_mfma_f32_16x16x32_f16 v[228:231], v[160:163], v[20:23], v[228:231]
	s_waitcnt lgkmcnt(4)
	v_mfma_f32_16x16x32_f16 v[200:203], v[124:127], v[24:27], v[200:203]
	v_mfma_f32_16x16x32_f16 v[232:235], v[164:167], v[24:27], v[232:235]
	s_waitcnt lgkmcnt(3)
	v_mfma_f32_16x16x32_f16 v[204:207], v[128:131], v[28:31], v[204:207]
	v_mfma_f32_16x16x32_f16 v[236:239], v[168:171], v[28:31], v[236:239]
	s_waitcnt lgkmcnt(2)
	v_mfma_f32_16x16x32_f16 v[208:211], v[132:135], v[32:35], v[208:211]
	v_mfma_f32_16x16x32_f16 v[240:243], v[172:175], v[32:35], v[240:243]
	s_waitcnt lgkmcnt(1)
	v_mfma_f32_16x16x32_f16 v[212:215], v[136:139], v[36:39], v[212:215]
	v_mfma_f32_16x16x32_f16 v[244:247], v[176:179], v[36:39], v[244:247]
	s_waitcnt lgkmcnt(0)
	v_mfma_f32_16x16x32_f16 v[216:219], v[140:143], v[40:43], v[216:219]
	v_mfma_f32_16x16x32_f16 v[248:251], v[180:183], v[40:43], v[248:251]
	s_mov_b32 s40, 0x348e00
	s_mov_b32 s41, 0x36aa90
	s_mov_b32 s42, 0x38c720
	s_mov_b32 s43, 0x3ae3b0
	s_mov_b32 s44, 0x3d0040
	s_mov_b32 s45, 0x3f1cd0
	s_mov_b32 s46, 0x413960
	s_mov_b32 s47, 0x4355f0
	buffer_load_dwordx2 v[92:93], v3, s[4:7], s40 offen nt
	buffer_load_dwordx2 v[94:95], v3, s[4:7], s41 offen nt
	buffer_load_dwordx2 v[96:97], v3, s[4:7], s42 offen nt
	buffer_load_dwordx2 v[98:99], v3, s[4:7], s43 offen nt
	buffer_load_dwordx2 v[100:101], v3, s[4:7], s44 offen nt
	buffer_load_dwordx2 v[102:103], v3, s[4:7], s45 offen nt
	buffer_load_dwordx2 v[104:105], v3, s[4:7], s46 offen nt
	buffer_load_dwordx2 v[106:107], v3, s[4:7], s47 offen nt
	s_waitcnt vmcnt(24)
	v_cvt_pkrtz_f16_f32 v12, v44, v46
	v_cvt_pkrtz_f16_f32 v13, v48, v50
	v_cvt_pkrtz_f16_f32 v14, v52, v54
	v_cvt_pkrtz_f16_f32 v15, v56, v58
	v_cvt_pkrtz_f16_f32 v16, v45, v47
	v_cvt_pkrtz_f16_f32 v17, v49, v51
	v_cvt_pkrtz_f16_f32 v18, v53, v55
	v_cvt_pkrtz_f16_f32 v19, v57, v59
	ds_write_b128 v5, v[12:15] offset:0
	ds_write_b128 v5, v[16:19] offset:2048
	s_waitcnt vmcnt(16)
	v_cvt_pkrtz_f16_f32 v12, v60, v62
	v_cvt_pkrtz_f16_f32 v13, v64, v66
	v_cvt_pkrtz_f16_f32 v14, v68, v70
	v_cvt_pkrtz_f16_f32 v15, v72, v74
	v_cvt_pkrtz_f16_f32 v16, v61, v63
	v_cvt_pkrtz_f16_f32 v17, v65, v67
	v_cvt_pkrtz_f16_f32 v18, v69, v71
	v_cvt_pkrtz_f16_f32 v19, v73, v75
	ds_write_b128 v5, v[12:15] offset:256
	ds_write_b128 v5, v[16:19] offset:2304
	s_waitcnt vmcnt(8)
	v_cvt_pkrtz_f16_f32 v12, v76, v78
	v_cvt_pkrtz_f16_f32 v13, v80, v82
	v_cvt_pkrtz_f16_f32 v14, v84, v86
	v_cvt_pkrtz_f16_f32 v15, v88, v90
	v_cvt_pkrtz_f16_f32 v16, v77, v79
	v_cvt_pkrtz_f16_f32 v17, v81, v83
	v_cvt_pkrtz_f16_f32 v18, v85, v87
	v_cvt_pkrtz_f16_f32 v19, v89, v91
	ds_write_b128 v5, v[12:15] offset:512
	ds_write_b128 v5, v[16:19] offset:2560
	s_waitcnt vmcnt(0)
	v_cvt_pkrtz_f16_f32 v12, v92, v94
	v_cvt_pkrtz_f16_f32 v13, v96, v98
	v_cvt_pkrtz_f16_f32 v14, v100, v102
	v_cvt_pkrtz_f16_f32 v15, v104, v106
	v_cvt_pkrtz_f16_f32 v16, v93, v95
	v_cvt_pkrtz_f16_f32 v17, v97, v99
	v_cvt_pkrtz_f16_f32 v18, v101, v103
	v_cvt_pkrtz_f16_f32 v19, v105, v107
	ds_write_b128 v5, v[12:15] offset:768
	ds_write_b128 v5, v[16:19] offset:2816
	s_waitcnt lgkmcnt(0)
	s_barrier
	ds_read_b128 v[12:15], v6 offset:0
	ds_read_b128 v[16:19], v6 offset:2048
	ds_read_b128 v[20:23], v7 offset:0
	ds_read_b128 v[24:27], v7 offset:2048
	ds_read_b128 v[28:31], v8 offset:0
	ds_read_b128 v[32:35], v8 offset:2048
	ds_read_b128 v[36:39], v9 offset:0
	ds_read_b128 v[40:43], v9 offset:2048
	s_waitcnt lgkmcnt(7)
	v_mfma_f32_16x16x32_f16 v[188:191], v[116:119], v[12:15], v[188:191]
	v_mfma_f32_16x16x32_f16 v[220:223], v[156:159], v[12:15], v[220:223]
	s_waitcnt lgkmcnt(6)
	v_mfma_f32_16x16x32_f16 v[192:195], v[120:123], v[16:19], v[192:195]
	v_mfma_f32_16x16x32_f16 v[224:227], v[160:163], v[16:19], v[224:227]
	s_waitcnt lgkmcnt(5)
	v_mfma_f32_16x16x32_f16 v[196:199], v[124:127], v[20:23], v[196:199]
	v_mfma_f32_16x16x32_f16 v[228:231], v[164:167], v[20:23], v[228:231]
	s_waitcnt lgkmcnt(4)
	v_mfma_f32_16x16x32_f16 v[200:203], v[128:131], v[24:27], v[200:203]
	v_mfma_f32_16x16x32_f16 v[232:235], v[168:171], v[24:27], v[232:235]
	s_waitcnt lgkmcnt(3)
	v_mfma_f32_16x16x32_f16 v[204:207], v[132:135], v[28:31], v[204:207]
	v_mfma_f32_16x16x32_f16 v[236:239], v[172:175], v[28:31], v[236:239]
	s_waitcnt lgkmcnt(2)
	v_mfma_f32_16x16x32_f16 v[208:211], v[136:139], v[32:35], v[208:211]
	v_mfma_f32_16x16x32_f16 v[240:243], v[176:179], v[32:35], v[240:243]
	s_waitcnt lgkmcnt(1)
	v_mfma_f32_16x16x32_f16 v[212:215], v[140:143], v[36:39], v[212:215]
	v_mfma_f32_16x16x32_f16 v[244:247], v[180:183], v[36:39], v[244:247]
	s_waitcnt lgkmcnt(0)
	v_mfma_f32_16x16x32_f16 v[216:219], v[144:147], v[40:43], v[216:219]
	v_mfma_f32_16x16x32_f16 v[248:251], v[184:187], v[40:43], v[248:251]
	s_nop 7
	s_nop 3
	v_and_b32_e32 v10, 1, v0
	v_cmp_eq_u32_e32 vcc, 1, v10
	s_nop 1
	v_cndmask_b32_e32 v188, v188, v220, vcc
	v_cndmask_b32_e32 v189, v189, v221, vcc
	v_cndmask_b32_e32 v190, v190, v222, vcc
	v_cndmask_b32_e32 v191, v191, v223, vcc
	v_cndmask_b32_e32 v192, v192, v224, vcc
	v_cndmask_b32_e32 v193, v193, v225, vcc
	v_cndmask_b32_e32 v194, v194, v226, vcc
	v_cndmask_b32_e32 v195, v195, v227, vcc
	v_cndmask_b32_e32 v196, v196, v228, vcc
	v_cndmask_b32_e32 v197, v197, v229, vcc
	v_cndmask_b32_e32 v198, v198, v230, vcc
	v_cndmask_b32_e32 v199, v199, v231, vcc
	v_cndmask_b32_e32 v200, v200, v232, vcc
	v_cndmask_b32_e32 v201, v201, v233, vcc
	v_cndmask_b32_e32 v202, v202, v234, vcc
	v_cndmask_b32_e32 v203, v203, v235, vcc
	v_cndmask_b32_e32 v204, v204, v236, vcc
	v_cndmask_b32_e32 v205, v205, v237, vcc
	v_cndmask_b32_e32 v206, v206, v238, vcc
	v_cndmask_b32_e32 v207, v207, v239, vcc
	v_cndmask_b32_e32 v208, v208, v240, vcc
	v_cndmask_b32_e32 v209, v209, v241, vcc
	v_cndmask_b32_e32 v210, v210, v242, vcc
	v_cndmask_b32_e32 v211, v211, v243, vcc
	v_cndmask_b32_e32 v212, v212, v244, vcc
	v_cndmask_b32_e32 v213, v213, v245, vcc
	v_cndmask_b32_e32 v214, v214, v246, vcc
	v_cndmask_b32_e32 v215, v215, v247, vcc
	v_cndmask_b32_e32 v216, v216, v248, vcc
	v_cndmask_b32_e32 v217, v217, v249, vcc
	v_cndmask_b32_e32 v218, v218, v250, vcc
	v_cndmask_b32_e32 v219, v219, v251, vcc
	s_barrier
	v_lshrrev_b32_e32 v10, 4, v2
	v_lshlrev_b32_e32 v10, 6, v10
	v_and_b32_e32 v12, 15, v2
	v_add_u32_e32 v10, v10, v12
	v_mul_u32_u24_e32 v10, 0x108, v10
	v_lshl_add_u32 v10, v1, 5, v10
	ds_write_b32 v10, v188 offset:0
	ds_write_b32 v10, v189 offset:4224
	ds_write_b32 v10, v190 offset:8448
	ds_write_b32 v10, v191 offset:12672
	ds_write_b32 v10, v192 offset:4
	ds_write_b32 v10, v193 offset:4228
	ds_write_b32 v10, v194 offset:8452
	ds_write_b32 v10, v195 offset:12676
	s_waitcnt lgkmcnt(4)
	ds_write_b32 v10, v196 offset:8
	ds_write_b32 v10, v197 offset:4232
	ds_write_b32 v10, v198 offset:8456
	ds_write_b32 v10, v199 offset:12680
	ds_write_b32 v10, v200 offset:12
	ds_write_b32 v10, v201 offset:4236
	ds_write_b32 v10, v202 offset:8460
	ds_write_b32 v10, v203 offset:12684
	s_waitcnt lgkmcnt(4)
	ds_write_b32 v10, v204 offset:16
	ds_write_b32 v10, v205 offset:4240
	ds_write_b32 v10, v206 offset:8464
	ds_write_b32 v10, v207 offset:12688
	ds_write_b32 v10, v208 offset:20
	ds_write_b32 v10, v209 offset:4244
	ds_write_b32 v10, v210 offset:8468
	ds_write_b32 v10, v211 offset:12692
	s_waitcnt lgkmcnt(4)
	ds_write_b32 v10, v212 offset:24
	ds_write_b32 v10, v213 offset:4248
	ds_write_b32 v10, v214 offset:8472
	ds_write_b32 v10, v215 offset:12696
	ds_write_b32 v10, v216 offset:28
	ds_write_b32 v10, v217 offset:4252
	ds_write_b32 v10, v218 offset:8476
	ds_write_b32 v10, v219 offset:12700
	s_waitcnt lgkmcnt(0)
	s_barrier
	v_lshrrev_b32_e32 v12, 5, v0
	v_mul_u32_u24_e32 v12, 0x108, v12
	v_and_b32_e32 v13, 31, v0
	v_lshl_add_u32 v12, v13, 3, v12
	ds_read_b64 v[44:45], v12 offset:0
	ds_read_b64 v[46:47], v12 offset:4224
	ds_read_b64 v[48:49], v12 offset:8448
	ds_read_b64 v[50:51], v12 offset:12672
	ds_read_b64 v[52:53], v12 offset:16896
	ds_read_b64 v[54:55], v12 offset:21120
	ds_read_b64 v[56:57], v12 offset:25344
	ds_read_b64 v[58:59], v12 offset:29568
	s_waitcnt lgkmcnt(7)
	v_add_f32_e32 v44, v252, v44
	v_add_f32_e32 v45, v253, v45
	s_mov_b32 s40, 0x0
	buffer_store_dwordx2 v[44:45], v11, s[32:35], s40 offen nt
	s_waitcnt lgkmcnt(6)
	v_add_f32_e32 v46, v252, v46
	v_add_f32_e32 v47, v253, v47
	s_mov_b32 s41, 0xf0400
	buffer_store_dwordx2 v[46:47], v11, s[32:35], s41 offen nt
	s_waitcnt lgkmcnt(5)
	v_add_f32_e32 v48, v252, v48
	v_add_f32_e32 v49, v253, v49
	s_mov_b32 s42, 0x1e0800
	buffer_store_dwordx2 v[48:49], v11, s[32:35], s42 offen nt
	s_waitcnt lgkmcnt(4)
	v_add_f32_e32 v50, v252, v50
	v_add_f32_e32 v51, v253, v51
	s_mov_b32 s43, 0x2d0c00
	buffer_store_dwordx2 v[50:51], v11, s[32:35], s43 offen nt
	s_waitcnt lgkmcnt(3)
	v_add_f32_e32 v52, v252, v52
	v_add_f32_e32 v53, v253, v53
	s_mov_b32 s44, 0x3c1000
	buffer_store_dwordx2 v[52:53], v11, s[32:35], s44 offen nt
	s_waitcnt lgkmcnt(2)
	v_add_f32_e32 v54, v252, v54
	v_add_f32_e32 v55, v253, v55
	s_mov_b32 s45, 0x4b1400
	buffer_store_dwordx2 v[54:55], v11, s[32:35], s45 offen nt
	s_waitcnt lgkmcnt(1)
	v_add_f32_e32 v56, v252, v56
	v_add_f32_e32 v57, v253, v57
	s_mov_b32 s46, 0x5a1800
	buffer_store_dwordx2 v[56:57], v11, s[32:35], s46 offen nt
	s_waitcnt lgkmcnt(0)
	v_add_f32_e32 v58, v252, v58
	v_add_f32_e32 v59, v253, v59
	s_mov_b32 s47, 0x691c00
	buffer_store_dwordx2 v[58:59], v11, s[32:35], s47 offen nt
	ds_read_b64 v[60:61], v12 offset:33792
	ds_read_b64 v[62:63], v12 offset:38016
	ds_read_b64 v[64:65], v12 offset:42240
	ds_read_b64 v[66:67], v12 offset:46464
	ds_read_b64 v[68:69], v12 offset:50688
	ds_read_b64 v[70:71], v12 offset:54912
	ds_read_b64 v[72:73], v12 offset:59136
	ds_read_b64 v[74:75], v12 offset:63360
	s_waitcnt lgkmcnt(7)
	v_add_f32_e32 v60, v252, v60
	v_add_f32_e32 v61, v253, v61
	s_mov_b32 s40, 0x782000
	buffer_store_dwordx2 v[60:61], v11, s[32:35], s40 offen nt
	s_waitcnt lgkmcnt(6)
	v_add_f32_e32 v62, v252, v62
	v_add_f32_e32 v63, v253, v63
	s_mov_b32 s41, 0x872400
	buffer_store_dwordx2 v[62:63], v11, s[32:35], s41 offen nt
	s_waitcnt lgkmcnt(5)
	v_add_f32_e32 v64, v252, v64
	v_add_f32_e32 v65, v253, v65
	s_mov_b32 s42, 0x962800
	buffer_store_dwordx2 v[64:65], v11, s[32:35], s42 offen nt
	s_waitcnt lgkmcnt(4)
	v_add_f32_e32 v66, v252, v66
	v_add_f32_e32 v67, v253, v67
	s_mov_b32 s43, 0xa52c00
	buffer_store_dwordx2 v[66:67], v11, s[32:35], s43 offen nt
	s_waitcnt lgkmcnt(3)
	v_add_f32_e32 v68, v252, v68
	v_add_f32_e32 v69, v253, v69
	s_mov_b32 s44, 0xb43000
	buffer_store_dwordx2 v[68:69], v11, s[32:35], s44 offen nt
	s_waitcnt lgkmcnt(2)
	v_add_f32_e32 v70, v252, v70
	v_add_f32_e32 v71, v253, v71
	s_mov_b32 s45, 0xc33400
	buffer_store_dwordx2 v[70:71], v11, s[32:35], s45 offen nt
	s_waitcnt lgkmcnt(1)
	v_add_f32_e32 v72, v252, v72
	v_add_f32_e32 v73, v253, v73
	s_mov_b32 s46, 0xd23800
	buffer_store_dwordx2 v[72:73], v11, s[32:35], s46 offen nt
	s_waitcnt lgkmcnt(0)
	v_add_f32_e32 v74, v252, v74
	v_add_f32_e32 v75, v253, v75
	s_mov_b32 s47, 0xe13c00
	buffer_store_dwordx2 v[74:75], v11, s[32:35], s47 offen nt
	s_endpgm
